# RWKV scan produce: the forward-substitution broadcasts are wave-uniform, so v_readlane into an SGPR (pipelined two terms ahead) feeds v_pk_fma instead of a DPP row-broadcast mov per term
# speedup vs baseline: 1.0015x; 1.0015x over previous
.LBB0_678:
	s_and_b64 vcc, exec, s[0:1]
	s_cbranch_vccz .LBB0_672
	s_add_i32 s25, s25, 1
	s_mul_i32 s6, s25, 6
	s_add_i32 s6, s6, s76
	s_cmpk_gt_u32 s6, 0x10f
	s_cbranch_scc1 .LBB0_673
	v_writelane_b32 v255, s70, 50
	v_writelane_b32 v255, s71, 51
	v_writelane_b32 v255, s72, 52
	v_writelane_b32 v255, s73, 53
	v_writelane_b32 v255, s74, 54
	v_writelane_b32 v255, s75, 55
	v_lshlrev_b32_e32 v4, 16, v143
	v_lshlrev_b32_e32 v6, 16, v145
	v_exp_f32_e64 v86, -v4
	v_exp_f32_e64 v6, -v6
	v_lshlrev_b32_e32 v10, 16, v148
	v_exp_f32_e64 v10, -v10
	v_lshlrev_b32_e32 v13, 16, v152
	v_exp_f32_e64 v14, -v13
	v_lshlrev_b32_e32 v15, 16, v155
	v_exp_f32_e64 v50, -v15
	v_lshlrev_b32_e32 v17, 16, v158
	v_exp_f32_e64 v52, -v17
	v_lshlrev_b32_e32 v54, 16, v161
	v_mul_f32_e32 v96, v86, v6
	v_exp_f32_e64 v54, -v54
	v_lshlrev_b32_e32 v56, 16, v163
	v_mul_f32_e32 v102, v10, v96
	v_exp_f32_e64 v56, -v56
	v_lshlrev_b32_e32 v58, 16, v167
	v_mul_f32_e32 v120, v14, v102
	v_exp_f32_e64 v58, -v58
	v_lshlrev_b32_e32 v60, 16, v170
	v_mul_f32_e32 v121, v50, v120
	s_bitcmp1_b32 s25, 0
	v_exp_f32_e64 v64, -v60
	v_lshlrev_b32_e32 v60, 16, v172
	v_mul_f32_e32 v124, v52, v121
	s_cselect_b32 s0, 6, 0
	v_exp_f32_e64 v84, -v60
	v_lshlrev_b32_e32 v60, 16, v175
	v_mul_f32_e32 v125, v54, v124
	s_add_i32 s0, s0, s76
	v_mov_b32_e32 v206, v0
	v_exp_f32_e64 v87, -v60
	v_lshlrev_b32_e32 v60, 16, v178
	v_mul_f32_e32 v182, v56, v125
	s_mulk_i32 s0, 0x2d00
	v_lshlrev_b32_e32 v2, 16, v140
	v_exp_f32_e64 v89, -v60
	v_lshlrev_b32_e32 v60, 16, v181
	v_mul_f32_e32 v183, v58, v182
	v_lshlrev_b32_e32 v208, 1, v206
	s_add_i32 s3, s0, 0
	v_lshlrev_b32_e32 v4, 16, v142
	v_lshlrev_b32_e32 v55, 16, v160
	v_exp_f32_e64 v91, -v60
	v_lshlrev_b32_e32 v60, 16, v186
	v_mul_f32_e32 v82, v86, v2
	v_mul_f32_e32 v210, v64, v183
	v_and_b32_e32 v54, 0x7e, v208
	v_lshlrev_b32_e32 v8, 16, v146
	v_exp_f32_e64 v93, -v60
	v_lshlrev_b32_e32 v60, 16, v189
	v_mul_f32_e32 v80, v96, v4
	v_mul_f32_e32 v68, v182, v55
	v_mul_f32_e32 v211, v84, v210
	v_add_u32_e32 v212, s3, v54
	v_cvt_pk_bf16_f32 v55, v82, s0
	v_lshlrev_b32_e32 v12, 16, v149
	v_lshlrev_b32_e32 v16, 16, v151
	v_exp_f32_e64 v95, -v60
	v_mul_f32_e32 v78, v102, v8
	v_mul_f32_e32 v103, v87, v211
	ds_write_b16 v212, v55 offset:3072
	v_xad_u32 v213, v54, 16, s3
	v_cvt_pk_bf16_f32 v55, v80, s0
	v_mul_f32_e32 v76, v120, v12
	v_mul_f32_e32 v74, v121, v16
	v_mul_f32_e32 v104, v89, v103
	ds_write_b16 v213, v55 offset:3200
	v_xad_u32 v214, v54, 32, s3
	v_cvt_pk_bf16_f32 v55, v78, s0
	v_lshlrev_b32_e32 v51, 16, v154
	v_mul_f32_e32 v2, v91, v104
	ds_write_b16 v214, v55 offset:3328
	v_xad_u32 v215, v54, 48, s3
	v_cvt_pk_bf16_f32 v55, v76, s0
	v_xad_u32 v105, v54, 64, s3
	v_cvt_pk_bf16_f32 v54, v74, s0
	s_movk_i32 s0, 0x50
	v_mul_f32_e32 v72, v124, v51
	v_mul_f32_e32 v64, v93, v2
	ds_write_b16 v105, v54 offset:3584
	v_bitop3_b32 v54, v208, s0, v239 bitop3:0x6c
	v_lshlrev_b32_e32 v53, 16, v157
	v_mul_f32_e32 v84, v95, v64
	v_add_u32_e32 v95, s3, v54
	v_cvt_pk_bf16_f32 v54, v72, s0
	s_movk_i32 s0, 0x60
	v_lshlrev_b32_e32 v65, 16, v169
	v_mul_f32_e32 v70, v125, v53
	ds_write_b16 v95, v54 offset:3712
	v_bitop3_b32 v54, v208, s0, v239 bitop3:0x6c
	v_mul_f32_e32 v14, v211, v65
	v_add_u32_e32 v65, s3, v54
	v_cvt_pk_bf16_f32 v54, v70, s0
	s_movk_i32 s0, 0x70
	v_lshlrev_b32_e32 v57, 16, v164
	v_lshlrev_b32_e32 v85, 16, v173
	ds_write_b16 v65, v54 offset:3840
	v_bitop3_b32 v54, v208, s0, v239 bitop3:0x6c
	v_lshlrev_b32_e32 v59, 16, v166
	v_mul_f32_e32 v66, v183, v57
	v_mul_f32_e32 v12, v103, v85
	v_add_u32_e32 v85, s3, v54
	v_cvt_pk_bf16_f32 v54, v68, s0
	v_mul_f32_e32 v16, v210, v59
	ds_write_b16 v85, v54 offset:3968
	v_cvt_pk_bf16_f32 v54, v66, s0
	ds_write_b16 v212, v54 offset:4096
	v_cvt_pk_bf16_f32 v54, v16, s0
	v_lshlrev_b32_e32 v88, 16, v176
	ds_write_b16 v213, v54 offset:4224
	v_cvt_pk_bf16_f32 v54, v14, s0
	v_lshlrev_b32_e32 v90, 16, v179
	v_mul_f32_e32 v10, v104, v88
	ds_write_b16 v214, v54 offset:4352
	v_cvt_pk_bf16_f32 v54, v12, s0
	v_lshlrev_b32_e32 v92, 16, v184
	v_mul_f32_e32 v8, v2, v90
	ds_write_b16 v215, v54 offset:4480
	v_cvt_pk_bf16_f32 v54, v10, s0
	v_lshlrev_b32_e32 v94, 16, v187
	v_mul_f32_e32 v6, v64, v92
	ds_write_b16 v105, v54 offset:4608
	v_cvt_pk_bf16_f32 v54, v8, s0
	v_mul_f32_e32 v4, v84, v94
	ds_write_b16 v95, v54 offset:4736
	v_cvt_pk_bf16_f32 v54, v6, s0
	ds_write_b16 v65, v54 offset:4864
	v_cvt_pk_bf16_f32 v54, v4, s0
	ds_write_b16 v85, v54 offset:4992
	v_bfe_u32 v89, v206, 5, 1
	v_lshlrev_b32_e32 v54, 7, v206
	v_and_b32_e32 v91, 0xf80, v54
	v_bitop3_b32 v54, v89, v206, 7 bitop3:0x78
	v_and_b32_e32 v93, 7, v206
	v_lshl_or_b32 v54, v54, 4, v91
	v_add_u32_e32 v97, s3, v54
	v_bitop3_b32 v54, v89, v93, 2 bitop3:0x36
	v_lshl_or_b32 v54, v54, 4, v91
	v_and_b32_e32 v111, 0xffff0000, v204
	v_lshlrev_b32_e32 v110, 16, v204
	ds_write_b16 v215, v55 offset:3456
	v_add_u32_e32 v87, s3, v54
	v_pk_mul_f32 v[54:55], v[98:99], v[110:111]
	v_rcp_f32_e32 v106, v86
	v_pk_mul_f32 v[112:113], v[54:55], v[54:55]
	v_rcp_f32_e32 v107, v96
	v_and_b32_e32 v119, 0xffff0000, v205
	v_add_f32_dpp v88, v112, v112 quad_perm:[1,0,3,2] row_mask:0xf bank_mask:0xf bound_ctrl:1
	v_lshlrev_b32_e32 v118, 16, v205
	v_rcp_f32_e32 v108, v102
	v_add_f32_dpp v88, v88, v88 quad_perm:[2,3,0,1] row_mask:0xf bank_mask:0xf bound_ctrl:1
	v_rcp_f32_e32 v109, v120
	v_rcp_f32_e32 v62, v121
	v_add_f32_dpp v88, v88, v88 row_half_mirror row_mask:0xf bank_mask:0xf bound_ctrl:1
	v_rcp_f32_e32 v63, v124
	v_rcp_f32_e32 v60, v125
	v_add_f32_dpp v88, v88, v88 row_mirror row_mask:0xf bank_mask:0xf bound_ctrl:1
	v_mov_b32_e32 v90, v88
	s_nop 1
	v_permlane16_swap_b32_e32 v88, v90
	v_add_f32_e32 v88, v88, v90
	v_mov_b32_e32 v90, v88
	s_nop 1
	v_permlane32_swap_b32_e32 v88, v90
	v_add_f32_e32 v88, v88, v90
	v_max_f32_e32 v88, 0x179abe15, v88
	v_rsq_f32_e32 v112, v88
	v_rcp_f32_e32 v61, v182
	v_add_f32_dpp v88, v113, v113 quad_perm:[1,0,3,2] row_mask:0xf bank_mask:0xf bound_ctrl:1
	v_rcp_f32_e32 v58, v183
	v_rcp_f32_e32 v59, v210
	v_add_f32_dpp v88, v88, v88 quad_perm:[2,3,0,1] row_mask:0xf bank_mask:0xf bound_ctrl:1
	v_rcp_f32_e32 v56, v211
	v_rcp_f32_e32 v57, v103
	v_add_f32_dpp v88, v88, v88 row_half_mirror row_mask:0xf bank_mask:0xf bound_ctrl:1
	v_rcp_f32_e32 v52, v104
	v_rcp_f32_e32 v53, v2
	v_add_f32_dpp v88, v88, v88 row_mirror row_mask:0xf bank_mask:0xf bound_ctrl:1
	v_mov_b32_e32 v90, v88
	s_nop 1
	v_permlane16_swap_b32_e32 v88, v90
	v_add_f32_e32 v88, v88, v90
	v_mov_b32_e32 v90, v88
	s_nop 1
	v_permlane32_swap_b32_e32 v88, v90
	v_add_f32_e32 v88, v88, v90
	v_max_f32_e32 v88, 0x179abe15, v88
	v_rsq_f32_e32 v113, v88
	v_rcp_f32_e32 v50, v64
	v_rcp_f32_e32 v51, v84
	v_bitop3_b32 v216, v89, v93, 4 bitop3:0x36
	v_pk_mul_f32 v[54:55], v[54:55], v[112:113]
	v_and_b32_e32 v207, 63, v206
	v_pk_mul_f32 v[112:113], v[54:55], v[118:119]
	v_mul_f32_e64 v86, v86, -v55
	v_pk_mul_f32 v[114:115], v[106:107], v[112:113]
	v_pk_add_f32 v[112:113], v[118:119], -1.0 op_sel_hi:[1,0]
	v_and_b32_e32 v119, 0xffff0000, v203
	v_pk_fma_f32 v[112:113], v[100:101], v[112:113], 1.0 op_sel_hi:[1,1,0]
	v_lshlrev_b32_e32 v118, 16, v203
	v_pk_mul_f32 v[110:111], v[112:113], v[110:111]
	v_cvt_pk_bf16_f32 v55, v114, s0
	v_pk_mul_f32 v[122:123], v[110:111], v[106:107]
	v_and_b32_e32 v107, 0xffff0000, v202
	v_lshlrev_b32_e32 v106, 16, v202
	v_pk_mul_f32 v[110:111], v[98:99], v[106:107]
	ds_write_b16 v212, v55 offset:5120
	v_pk_mul_f32 v[112:113], v[110:111], v[110:111]
	v_cvt_pk_bf16_f32 v55, v86, s0
	ds_write_b16 v213, v55 offset:1152
	v_add_f32_dpp v88, v112, v112 quad_perm:[1,0,3,2] row_mask:0xf bank_mask:0xf bound_ctrl:1
	v_cvt_pk_bf16_f32 v55, v115, s0
	ds_write_b16 v213, v55 offset:5248
	v_add_f32_dpp v88, v88, v88 quad_perm:[2,3,0,1] row_mask:0xf bank_mask:0xf bound_ctrl:1
	v_cvt_pk_bf16_f32 v55, v122, s0
	ds_write_b16 v212, v55 offset:7168
	v_add_f32_dpp v88, v88, v88 row_half_mirror row_mask:0xf bank_mask:0xf bound_ctrl:1
	v_cvt_pk_bf16_f32 v55, v123, s0
	ds_write_b16 v213, v55 offset:7296
	v_add_f32_dpp v88, v88, v88 row_mirror row_mask:0xf bank_mask:0xf bound_ctrl:1
	v_mov_b32_e32 v90, v88
	s_nop 1
	v_permlane16_swap_b32_e32 v88, v90
	v_add_f32_e32 v88, v88, v90
	v_mov_b32_e32 v90, v88
	s_nop 1
	v_permlane32_swap_b32_e32 v88, v90
	v_add_f32_e32 v88, v88, v90
	v_max_f32_e32 v88, 0x179abe15, v88
	v_rsq_f32_e32 v112, v88
	v_cvt_pk_bf16_f32 v209, -v54, s0
	v_add_f32_dpp v88, v113, v113 quad_perm:[1,0,3,2] row_mask:0xf bank_mask:0xf bound_ctrl:1
	ds_write_b16 v212, v209 offset:1024
	v_lshlrev_b32_e32 v5, 16, v141
	v_add_f32_dpp v88, v88, v88 quad_perm:[2,3,0,1] row_mask:0xf bank_mask:0xf bound_ctrl:1
	v_lshlrev_b32_e32 v7, 16, v144
	v_lshlrev_b32_e32 v9, 16, v147
	v_add_f32_dpp v88, v88, v88 row_half_mirror row_mask:0xf bank_mask:0xf bound_ctrl:1
	v_lshlrev_b32_e32 v11, 16, v150
	v_lshlrev_b32_e32 v13, 16, v153
	v_add_f32_dpp v88, v88, v88 row_mirror row_mask:0xf bank_mask:0xf bound_ctrl:1
	v_mov_b32_e32 v90, v88
	s_nop 1
	v_permlane16_swap_b32_e32 v88, v90
	v_add_f32_e32 v88, v88, v90
	v_mov_b32_e32 v90, v88
	s_nop 1
	v_permlane32_swap_b32_e32 v88, v90
	v_add_f32_e32 v88, v88, v90
	v_max_f32_e32 v88, 0x179abe15, v88
	v_rsq_f32_e32 v113, v88
	v_lshlrev_b32_e32 v15, 16, v156
	v_lshlrev_b32_e32 v17, 16, v159
	v_lshlrev_b32_e32 v69, 16, v162
	v_pk_mul_f32 v[110:111], v[110:111], v[112:113]
	v_lshlrev_b32_e32 v67, 16, v165
	v_mul_f32_e64 v90, v96, -v110
	v_pk_mul_f32 v[112:113], v[110:111], v[118:119]
	v_mul_f32_e64 v88, v102, -v111
	v_pk_add_f32 v[110:111], v[118:119], -1.0 op_sel_hi:[1,0]
	v_pk_mul_f32 v[126:127], v[108:109], v[112:113]
	v_pk_fma_f32 v[110:111], v[100:101], v[110:111], 1.0 op_sel_hi:[1,1,0]
	v_and_b32_e32 v113, 0xffff0000, v197
	v_pk_mul_f32 v[106:107], v[110:111], v[106:107]
	v_lshlrev_b32_e32 v112, 16, v197
	v_pk_mul_f32 v[128:129], v[106:107], v[108:109]
	v_and_b32_e32 v107, 0xffff0000, v196
	v_lshlrev_b32_e32 v106, 16, v196
	v_pk_mul_f32 v[108:109], v[98:99], v[106:107]
	v_cvt_pk_bf16_f32 v55, v90, s0
	v_pk_mul_f32 v[110:111], v[108:109], v[108:109]
	ds_write_b16 v214, v55 offset:1280
	v_cvt_pk_bf16_f32 v55, v126, s0
	v_add_f32_dpp v92, v110, v110 quad_perm:[1,0,3,2] row_mask:0xf bank_mask:0xf bound_ctrl:1
	ds_write_b16 v214, v55 offset:5376
	v_cvt_pk_bf16_f32 v55, v88, s0
	v_add_f32_dpp v92, v92, v92 quad_perm:[2,3,0,1] row_mask:0xf bank_mask:0xf bound_ctrl:1
	ds_write_b16 v215, v55 offset:1408
	v_cvt_pk_bf16_f32 v55, v127, s0
	v_add_f32_dpp v92, v92, v92 row_half_mirror row_mask:0xf bank_mask:0xf bound_ctrl:1
	ds_write_b16 v215, v55 offset:5504
	v_cvt_pk_bf16_f32 v55, v128, s0
	v_add_f32_dpp v92, v92, v92 row_mirror row_mask:0xf bank_mask:0xf bound_ctrl:1
	v_mov_b32_e32 v94, v92
	s_nop 1
	v_permlane16_swap_b32_e32 v92, v94
	v_add_f32_e32 v92, v92, v94
	v_mov_b32_e32 v94, v92
	s_nop 1
	v_permlane32_swap_b32_e32 v92, v94
	v_add_f32_e32 v92, v92, v94
	v_max_f32_e32 v92, 0x179abe15, v92
	v_rsq_f32_e32 v110, v92
	ds_write_b16 v214, v55 offset:7424
	v_add_f32_dpp v92, v111, v111 quad_perm:[1,0,3,2] row_mask:0xf bank_mask:0xf bound_ctrl:1
	v_cvt_pk_bf16_f32 v55, v129, s0
	ds_write_b16 v215, v55 offset:7552
	v_add_f32_dpp v92, v92, v92 quad_perm:[2,3,0,1] row_mask:0xf bank_mask:0xf bound_ctrl:1
	v_lshlrev_b32_e32 v71, 16, v168
	v_lshlrev_b32_e32 v73, 16, v171
	v_add_f32_dpp v92, v92, v92 row_half_mirror row_mask:0xf bank_mask:0xf bound_ctrl:1
	v_lshlrev_b32_e32 v75, 16, v174
	v_lshlrev_b32_e32 v77, 16, v177
	v_add_f32_dpp v92, v92, v92 row_mirror row_mask:0xf bank_mask:0xf bound_ctrl:1
	v_mov_b32_e32 v94, v92
	s_nop 1
	v_permlane16_swap_b32_e32 v92, v94
	v_add_f32_e32 v92, v92, v94
	v_mov_b32_e32 v94, v92
	s_nop 1
	v_permlane32_swap_b32_e32 v92, v94
	v_add_f32_e32 v92, v92, v94
	v_max_f32_e32 v92, 0x179abe15, v92
	v_rsq_f32_e32 v111, v92
	v_lshlrev_b32_e32 v79, 16, v180
	v_lshlrev_b32_e32 v81, 16, v185
	v_lshlrev_b32_e32 v83, 16, v188
	v_pk_mul_f32 v[108:109], v[108:109], v[110:111]
	s_nop 0
	v_mul_f32_e64 v94, v120, -v108
	v_pk_mul_f32 v[110:111], v[108:109], v[112:113]
	v_mul_f32_e64 v92, v121, -v109
	v_pk_add_f32 v[108:109], v[112:113], -1.0 op_sel_hi:[1,0]
	v_pk_mul_f32 v[130:131], v[62:63], v[110:111]
	v_pk_fma_f32 v[108:109], v[100:101], v[108:109], 1.0 op_sel_hi:[1,1,0]
	v_and_b32_e32 v111, 0xffff0000, v195
	v_pk_mul_f32 v[106:107], v[108:109], v[106:107]
	v_lshlrev_b32_e32 v110, 16, v195
	v_pk_mul_f32 v[132:133], v[106:107], v[62:63]
	v_and_b32_e32 v63, 0xffff0000, v194
	v_lshlrev_b32_e32 v62, 16, v194
	v_pk_mul_f32 v[106:107], v[98:99], v[62:63]
	v_cvt_pk_bf16_f32 v55, v94, s0
	v_pk_mul_f32 v[108:109], v[106:107], v[106:107]
	ds_write_b16 v105, v55 offset:1536
	v_cvt_pk_bf16_f32 v55, v130, s0
	v_add_f32_dpp v96, v108, v108 quad_perm:[1,0,3,2] row_mask:0xf bank_mask:0xf bound_ctrl:1
	ds_write_b16 v105, v55 offset:5632
	v_cvt_pk_bf16_f32 v55, v92, s0
	v_add_f32_dpp v96, v96, v96 quad_perm:[2,3,0,1] row_mask:0xf bank_mask:0xf bound_ctrl:1
	ds_write_b16 v95, v55 offset:1664
	v_cvt_pk_bf16_f32 v55, v131, s0
	v_add_f32_dpp v96, v96, v96 row_half_mirror row_mask:0xf bank_mask:0xf bound_ctrl:1
	ds_write_b16 v95, v55 offset:5760
	v_cvt_pk_bf16_f32 v55, v132, s0
	v_add_f32_dpp v96, v96, v96 row_mirror row_mask:0xf bank_mask:0xf bound_ctrl:1
	v_mov_b32_e32 v102, v96
	s_nop 1
	v_permlane16_swap_b32_e32 v96, v102
	v_add_f32_e32 v96, v96, v102
	v_mov_b32_e32 v102, v96
	s_nop 1
	v_permlane32_swap_b32_e32 v96, v102
	v_add_f32_e32 v96, v96, v102
	v_max_f32_e32 v96, 0x179abe15, v96
	v_rsq_f32_e32 v108, v96
	ds_write_b16 v105, v55 offset:7680
	v_add_f32_dpp v96, v109, v109 quad_perm:[1,0,3,2] row_mask:0xf bank_mask:0xf bound_ctrl:1
	v_cvt_pk_bf16_f32 v55, v133, s0
	ds_write_b16 v95, v55 offset:7808
	v_add_f32_dpp v96, v96, v96 quad_perm:[2,3,0,1] row_mask:0xf bank_mask:0xf bound_ctrl:1
	s_nop 1
	v_add_f32_dpp v96, v96, v96 row_half_mirror row_mask:0xf bank_mask:0xf bound_ctrl:1
	s_nop 1
	v_add_f32_dpp v96, v96, v96 row_mirror row_mask:0xf bank_mask:0xf bound_ctrl:1
	v_mov_b32_e32 v102, v96
	s_nop 1
	v_permlane16_swap_b32_e32 v96, v102
	v_add_f32_e32 v96, v96, v102
	v_mov_b32_e32 v102, v96
	s_nop 1
	v_permlane32_swap_b32_e32 v96, v102
	v_add_f32_e32 v96, v96, v102
	v_max_f32_e32 v96, 0x179abe15, v96
	v_rsq_f32_e32 v109, v96
	s_nop 0
	v_pk_mul_f32 v[106:107], v[106:107], v[108:109]
	s_nop 0
	v_mul_f32_e64 v118, v124, -v106
	v_pk_mul_f32 v[108:109], v[106:107], v[110:111]
	v_mul_f32_e64 v96, v125, -v107
	v_pk_add_f32 v[106:107], v[110:111], -1.0 op_sel_hi:[1,0]
	v_pk_mul_f32 v[134:135], v[60:61], v[108:109]
	v_pk_fma_f32 v[106:107], v[100:101], v[106:107], 1.0 op_sel_hi:[1,1,0]
	v_and_b32_e32 v109, 0xffff0000, v201
	v_pk_mul_f32 v[62:63], v[106:107], v[62:63]
	v_lshlrev_b32_e32 v108, 16, v201
	v_pk_mul_f32 v[136:137], v[62:63], v[60:61]
	v_and_b32_e32 v61, 0xffff0000, v200
	v_lshlrev_b32_e32 v60, 16, v200
	v_pk_mul_f32 v[62:63], v[98:99], v[60:61]
	v_cvt_pk_bf16_f32 v55, v118, s0
	v_pk_mul_f32 v[106:107], v[62:63], v[62:63]
	ds_write_b16 v65, v55 offset:1792
	v_cvt_pk_bf16_f32 v55, v134, s0
	v_add_f32_dpp v102, v106, v106 quad_perm:[1,0,3,2] row_mask:0xf bank_mask:0xf bound_ctrl:1
	ds_write_b16 v65, v55 offset:5888
	v_cvt_pk_bf16_f32 v55, v96, s0
	v_add_f32_dpp v102, v102, v102 quad_perm:[2,3,0,1] row_mask:0xf bank_mask:0xf bound_ctrl:1
	ds_write_b16 v85, v55 offset:1920
	v_cvt_pk_bf16_f32 v55, v135, s0
	v_add_f32_dpp v102, v102, v102 row_half_mirror row_mask:0xf bank_mask:0xf bound_ctrl:1
	ds_write_b16 v85, v55 offset:6016
	v_cvt_pk_bf16_f32 v55, v136, s0
	v_add_f32_dpp v102, v102, v102 row_mirror row_mask:0xf bank_mask:0xf bound_ctrl:1
	v_mov_b32_e32 v106, v102
	s_nop 1
	v_permlane16_swap_b32_e32 v102, v106
	v_add_f32_e32 v102, v102, v106
	v_mov_b32_e32 v106, v102
	s_nop 1
	v_permlane32_swap_b32_e32 v102, v106
	v_add_f32_e32 v102, v102, v106
	v_max_f32_e32 v102, 0x179abe15, v102
	v_rsq_f32_e32 v106, v102
	ds_write_b16 v65, v55 offset:7936
	v_add_f32_dpp v102, v107, v107 quad_perm:[1,0,3,2] row_mask:0xf bank_mask:0xf bound_ctrl:1
	v_cvt_pk_bf16_f32 v55, v137, s0
	ds_write_b16 v85, v55 offset:8064
	v_add_f32_dpp v102, v102, v102 quad_perm:[2,3,0,1] row_mask:0xf bank_mask:0xf bound_ctrl:1
	s_nop 1
	v_add_f32_dpp v102, v102, v102 row_half_mirror row_mask:0xf bank_mask:0xf bound_ctrl:1
	s_nop 1
	v_add_f32_dpp v102, v102, v102 row_mirror row_mask:0xf bank_mask:0xf bound_ctrl:1
	v_mov_b32_e32 v107, v102
	s_nop 1
	v_permlane16_swap_b32_e32 v102, v107
	v_add_f32_e32 v102, v102, v107
	v_mov_b32_e32 v107, v102
	s_nop 1
	v_permlane32_swap_b32_e32 v102, v107
	v_add_f32_e32 v102, v102, v107
	v_max_f32_e32 v102, 0x179abe15, v102
	v_rsq_f32_e32 v107, v102
	s_nop 0
	v_pk_mul_f32 v[62:63], v[62:63], v[106:107]
	s_nop 0
	v_mul_f32_e64 v124, v182, -v62
	v_pk_mul_f32 v[106:107], v[62:63], v[108:109]
	v_mul_f32_e64 v110, v183, -v63
	v_pk_add_f32 v[62:63], v[108:109], -1.0 op_sel_hi:[1,0]
	v_pk_mul_f32 v[182:183], v[58:59], v[106:107]
	v_pk_fma_f32 v[62:63], v[100:101], v[62:63], 1.0 op_sel_hi:[1,1,0]
	v_and_b32_e32 v107, 0xffff0000, v199
	v_pk_mul_f32 v[60:61], v[62:63], v[60:61]
	v_lshlrev_b32_e32 v106, 16, v199
	v_pk_mul_f32 v[218:219], v[60:61], v[58:59]
	v_and_b32_e32 v59, 0xffff0000, v198
	v_lshlrev_b32_e32 v58, 16, v198
	v_pk_mul_f32 v[60:61], v[98:99], v[58:59]
	v_cvt_pk_bf16_f32 v55, v124, s0
	v_pk_mul_f32 v[62:63], v[60:61], v[60:61]
	ds_write_b16 v212, v55 offset:2048
	v_cvt_pk_bf16_f32 v55, v182, s0
	v_add_f32_dpp v62, v62, v62 quad_perm:[1,0,3,2] row_mask:0xf bank_mask:0xf bound_ctrl:1
	v_add_f32_dpp v63, v63, v63 quad_perm:[1,0,3,2] row_mask:0xf bank_mask:0xf bound_ctrl:1
	ds_write_b16 v212, v55 offset:6144
	v_add_f32_dpp v62, v62, v62 quad_perm:[2,3,0,1] row_mask:0xf bank_mask:0xf bound_ctrl:1
	v_add_f32_dpp v63, v63, v63 quad_perm:[2,3,0,1] row_mask:0xf bank_mask:0xf bound_ctrl:1
	v_cvt_pk_bf16_f32 v55, v110, s0
	v_add_f32_dpp v62, v62, v62 row_half_mirror row_mask:0xf bank_mask:0xf bound_ctrl:1
	v_add_f32_dpp v63, v63, v63 row_half_mirror row_mask:0xf bank_mask:0xf bound_ctrl:1
	ds_write_b16 v213, v55 offset:2176
	v_add_f32_dpp v62, v62, v62 row_mirror row_mask:0xf bank_mask:0xf bound_ctrl:1
	v_mov_b32_e32 v102, v62
	s_nop 1
	v_permlane16_swap_b32_e32 v62, v102
	v_add_f32_e32 v62, v62, v102
	v_mov_b32_e32 v102, v62
	s_nop 1
	v_permlane32_swap_b32_e32 v62, v102
	v_add_f32_dpp v63, v63, v63 row_mirror row_mask:0xf bank_mask:0xf bound_ctrl:1
	v_add_f32_e32 v62, v62, v102
	v_mov_b32_e32 v102, v63
	s_nop 1
	v_permlane16_swap_b32_e32 v63, v102
	v_add_f32_e32 v63, v63, v102
	v_mov_b32_e32 v102, v63
	s_nop 1
	v_permlane32_swap_b32_e32 v63, v102
	v_add_f32_e32 v63, v63, v102
	v_max_f32_e32 v62, 0x179abe15, v62
	v_max_f32_e32 v63, 0x179abe15, v63
	v_rsq_f32_e32 v62, v62
	v_rsq_f32_e32 v63, v63
	v_cvt_pk_bf16_f32 v55, v183, s0
	ds_write_b16 v213, v55 offset:6272
	v_cvt_pk_bf16_f32 v55, v218, s0
	v_pk_mul_f32 v[60:61], v[60:61], v[62:63]
	ds_write_b16 v212, v55 offset:8192
	v_mul_f32_e64 v120, v210, -v60
	v_pk_mul_f32 v[62:63], v[60:61], v[106:107]
	v_mul_f32_e64 v102, v211, -v61
	v_pk_add_f32 v[60:61], v[106:107], -1.0 op_sel_hi:[1,0]
	v_pk_mul_f32 v[220:221], v[56:57], v[62:63]
	v_pk_fma_f32 v[60:61], v[100:101], v[60:61], 1.0 op_sel_hi:[1,1,0]
	v_and_b32_e32 v63, 0xffff0000, v193
	v_pk_mul_f32 v[58:59], v[60:61], v[58:59]
	v_cvt_pk_bf16_f32 v55, v219, s0
	v_pk_mul_f32 v[222:223], v[58:59], v[56:57]
	v_and_b32_e32 v57, 0xffff0000, v192
	v_lshlrev_b32_e32 v56, 16, v192
	v_pk_mul_f32 v[58:59], v[98:99], v[56:57]
	ds_write_b16 v213, v55 offset:8320
	v_pk_mul_f32 v[60:61], v[58:59], v[58:59]
	v_cvt_pk_bf16_f32 v55, v120, s0
	ds_write_b16 v214, v55 offset:2304
	v_add_f32_dpp v60, v60, v60 quad_perm:[1,0,3,2] row_mask:0xf bank_mask:0xf bound_ctrl:1
	v_add_f32_dpp v61, v61, v61 quad_perm:[1,0,3,2] row_mask:0xf bank_mask:0xf bound_ctrl:1
	v_cvt_pk_bf16_f32 v55, v220, s0
	v_add_f32_dpp v60, v60, v60 quad_perm:[2,3,0,1] row_mask:0xf bank_mask:0xf bound_ctrl:1
	v_add_f32_dpp v61, v61, v61 quad_perm:[2,3,0,1] row_mask:0xf bank_mask:0xf bound_ctrl:1
	ds_write_b16 v214, v55 offset:6400
	v_add_f32_dpp v60, v60, v60 row_half_mirror row_mask:0xf bank_mask:0xf bound_ctrl:1
	v_add_f32_dpp v61, v61, v61 row_half_mirror row_mask:0xf bank_mask:0xf bound_ctrl:1
	v_cvt_pk_bf16_f32 v55, v102, s0
	v_add_f32_dpp v60, v60, v60 row_mirror row_mask:0xf bank_mask:0xf bound_ctrl:1
	v_mov_b32_e32 v62, v60
	s_nop 1
	v_permlane16_swap_b32_e32 v60, v62
	v_add_f32_e32 v60, v60, v62
	v_mov_b32_e32 v62, v60
	s_nop 1
	v_permlane32_swap_b32_e32 v60, v62
	v_add_f32_dpp v61, v61, v61 row_mirror row_mask:0xf bank_mask:0xf bound_ctrl:1
	v_add_f32_e32 v60, v60, v62
	v_mov_b32_e32 v62, v61
	s_nop 1
	v_permlane16_swap_b32_e32 v61, v62
	v_add_f32_e32 v61, v61, v62
	v_mov_b32_e32 v62, v61
	s_nop 1
	v_permlane32_swap_b32_e32 v61, v62
	v_add_f32_e32 v61, v61, v62
	v_max_f32_e32 v60, 0x179abe15, v60
	v_max_f32_e32 v61, 0x179abe15, v61
	v_rsq_f32_e32 v60, v60
	v_rsq_f32_e32 v61, v61
	v_lshlrev_b32_e32 v62, 16, v193
	ds_write_b16 v215, v55 offset:2432
	v_cvt_pk_bf16_f32 v55, v221, s0
	v_pk_mul_f32 v[58:59], v[58:59], v[60:61]
	ds_write_b16 v215, v55 offset:6528
	v_mul_f32_e64 v112, v103, -v58
	v_pk_mul_f32 v[60:61], v[58:59], v[62:63]
	v_mul_f32_e64 v104, v104, -v59
	v_pk_add_f32 v[58:59], v[62:63], -1.0 op_sel_hi:[1,0]
	v_pk_mul_f32 v[224:225], v[52:53], v[60:61]
	v_pk_fma_f32 v[58:59], v[100:101], v[58:59], 1.0 op_sel_hi:[1,1,0]
	v_and_b32_e32 v61, 0xffff0000, v191
	v_pk_mul_f32 v[56:57], v[58:59], v[56:57]
	v_cvt_pk_bf16_f32 v55, v222, s0
	v_pk_mul_f32 v[230:231], v[56:57], v[52:53]
	v_and_b32_e32 v53, 0xffff0000, v190
	v_cvt_pk_bf16_f32 v52, v230, s0
	ds_write_b16 v105, v52 offset:8704
	v_lshlrev_b32_e32 v52, 16, v190
	v_pk_mul_f32 v[56:57], v[98:99], v[52:53]
	ds_write_b16 v214, v55 offset:8448
	v_pk_mul_f32 v[58:59], v[56:57], v[56:57]
	v_cvt_pk_bf16_f32 v55, v223, s0
	ds_write_b16 v215, v55 offset:8576
	v_add_f32_dpp v58, v58, v58 quad_perm:[1,0,3,2] row_mask:0xf bank_mask:0xf bound_ctrl:1
	v_add_f32_dpp v59, v59, v59 quad_perm:[1,0,3,2] row_mask:0xf bank_mask:0xf bound_ctrl:1
	v_cvt_pk_bf16_f32 v55, v112, s0
	v_add_f32_dpp v58, v58, v58 quad_perm:[2,3,0,1] row_mask:0xf bank_mask:0xf bound_ctrl:1
	v_add_f32_dpp v59, v59, v59 quad_perm:[2,3,0,1] row_mask:0xf bank_mask:0xf bound_ctrl:1
	ds_write_b16 v105, v55 offset:2560
	v_add_f32_dpp v58, v58, v58 row_half_mirror row_mask:0xf bank_mask:0xf bound_ctrl:1
	v_add_f32_dpp v59, v59, v59 row_half_mirror row_mask:0xf bank_mask:0xf bound_ctrl:1
	v_cvt_pk_bf16_f32 v55, v224, s0
	v_add_f32_dpp v58, v58, v58 row_mirror row_mask:0xf bank_mask:0xf bound_ctrl:1
	v_mov_b32_e32 v60, v58
	s_nop 1
	v_permlane16_swap_b32_e32 v58, v60
	v_add_f32_e32 v58, v58, v60
	v_mov_b32_e32 v60, v58
	s_nop 1
	v_permlane32_swap_b32_e32 v58, v60
	v_add_f32_dpp v59, v59, v59 row_mirror row_mask:0xf bank_mask:0xf bound_ctrl:1
	v_add_f32_e32 v58, v58, v60
	v_mov_b32_e32 v60, v59
	s_nop 1
	v_permlane16_swap_b32_e32 v59, v60
	v_add_f32_e32 v59, v59, v60
	v_mov_b32_e32 v60, v59
	s_nop 1
	v_permlane32_swap_b32_e32 v59, v60
	v_add_f32_e32 v59, v59, v60
	v_max_f32_e32 v58, 0x179abe15, v58
	v_max_f32_e32 v59, 0x179abe15, v59
	v_rsq_f32_e32 v58, v58
	v_rsq_f32_e32 v59, v59
	v_lshlrev_b32_e32 v60, 16, v191
	ds_write_b16 v105, v55 offset:6656
	v_cvt_pk_bf16_f32 v55, v104, s0
	v_pk_mul_f32 v[56:57], v[56:57], v[58:59]
	ds_write_b16 v95, v55 offset:2688
	v_mul_f32_e64 v106, v2, -v56
	v_pk_mul_f32 v[58:59], v[56:57], v[60:61]
	v_mul_f32_e64 v108, v64, -v57
	v_pk_mul_f32 v[232:233], v[50:51], v[58:59]
	v_cvt_pk_bf16_f32 v2, v106, s0
	v_pk_add_f32 v[56:57], v[60:61], -1.0 op_sel_hi:[1,0]
	ds_write_b16 v65, v2 offset:2816
	v_cvt_pk_bf16_f32 v2, v232, s0
	v_pk_fma_f32 v[56:57], v[100:101], v[56:57], 1.0 op_sel_hi:[1,1,0]
	ds_write_b16 v65, v2 offset:6912
	v_cvt_pk_bf16_f32 v2, v108, s0
	v_pk_mul_f32 v[52:53], v[56:57], v[52:53]
	ds_write_b16 v85, v2 offset:2944
	v_cvt_pk_bf16_f32 v2, v233, s0
	v_pk_mul_f32 v[234:235], v[52:53], v[50:51]
	v_cvt_pk_bf16_f32 v55, v225, s0
	ds_write_b16 v85, v2 offset:7040
	v_cvt_pk_bf16_f32 v2, v234, s0
	ds_write_b16 v95, v55 offset:6784
	v_cvt_pk_bf16_f32 v55, v231, s0
	ds_write_b16 v65, v2 offset:8960
	v_cvt_pk_bf16_f32 v2, v235, s0
	ds_write_b16 v95, v55 offset:8832
	ds_write_b16 v85, v2 offset:9088
	s_waitcnt lgkmcnt(0)
	ds_read_b128 v[50:53], v97 offset:1024
	ds_read_b128 v[56:59], v97 offset:5120
	v_lshl_or_b32 v2, v216, 4, v91
	v_add_u32_e32 v85, s3, v2
	v_bitop3_b32 v2, v89, v93, 6 bitop3:0x36
	v_lshl_or_b32 v2, v2, 4, v91
	ds_read_b128 v[210:213], v87 offset:1024
	ds_read_b128 v[214:217], v87 offset:5120
	v_add_u32_e32 v89, s3, v2
	v_xor_b32_e32 v2, 0x80000000, v54
	s_waitcnt lgkmcnt(2)
	v_mfma_f32_32x32x16_bf16 v[50:65], v[50:53], v[56:59], 0
	v_mul_f32_e64 v236, v84, v126
	v_mul_f32_e64 v237, v84, v127
	v_mul_f32_e64 v240, v128, v84
	v_mul_f32_e64 v241, v129, v84
	ds_read_b128 v[126:129], v85 offset:1024
	v_pk_mul_f32 v[242:243], v[84:85], v[130:131] op_sel_hi:[0,1]
	v_pk_mul_f32 v[114:115], v[84:85], v[114:115] op_sel_hi:[0,1]
	v_pk_mul_f32 v[182:183], v[84:85], v[182:183] op_sel_hi:[0,1]
	v_pk_mul_f32 v[122:123], v[122:123], v[84:85] op_sel_hi:[1,0]
	s_waitcnt lgkmcnt(1)
	v_mfma_f32_32x32x16_bf16 v[50:65], v[210:213], v[214:217], v[50:65]
	v_mul_f32_e64 v210, v132, v84
	v_mul_f32_e64 v211, v133, v84
	ds_read_b128 v[130:133], v85 offset:5120
	v_mul_f32_e64 v212, v84, v134
	v_mul_f32_e64 v213, v84, v135
	v_pk_mul_f32 v[214:215], v[136:137], v[84:85] op_sel_hi:[1,0]
	ds_read_b128 v[134:137], v89 offset:1024
	v_pk_mul_f32 v[216:217], v[218:219], v[84:85] op_sel_hi:[1,0]
	v_pk_mul_f32 v[218:219], v[222:223], v[84:85] op_sel_hi:[1,0]
	s_waitcnt lgkmcnt(1)
	v_mfma_f32_32x32x16_bf16 v[50:65], v[126:129], v[130:133], v[50:65]
	ds_read_b128 v[126:129], v89 offset:5120
	v_mul_f32_e64 v130, v84, v220
	v_mul_f32_e64 v131, v84, v221
	v_mul_f32_e64 v132, v84, v224
	v_mul_f32_e64 v133, v84, v225
	v_pk_mul_f32 v[220:221], v[84:85], v[230:231] op_sel_hi:[0,1]
	v_pk_mul_f32 v[222:223], v[84:85], v[232:233] op_sel_hi:[0,1]
	v_pk_mul_f32 v[224:225], v[84:85], v[234:235] op_sel_hi:[0,1]
	v_lshl_add_u32 v85, v207, 5, s3
	s_waitcnt lgkmcnt(0)
	v_mfma_f32_32x32x16_bf16 v[50:65], v[134:137], v[126:129], v[50:65]
	v_cvt_pk_bf16_f32 v126, v114, v115
	v_cvt_pk_bf16_f32 v127, v236, v237
	v_cvt_pk_bf16_f32 v128, v182, v183
	v_cvt_pk_bf16_f32 v129, v130, v131
	v_cvt_pk_bf16_f32 v130, v242, v243
	v_cvt_pk_bf16_f32 v131, v212, v213
	v_cvt_pk_bf16_f32 v132, v132, v133
	v_cvt_pk_bf16_f32 v133, v222, v223
	ds_write_b128 v85, v[126:129] offset:5120
	ds_write_b128 v85, v[130:133] offset:5136
	v_cvt_pk_bf16_f32 v126, v122, v123
	v_cvt_pk_bf16_f32 v127, v240, v241
	v_cvt_pk_bf16_f32 v128, v210, v211
	v_cvt_pk_bf16_f32 v129, v214, v215
	v_cvt_pk_bf16_f32 v130, v216, v217
	v_cvt_pk_bf16_f32 v131, v218, v219
	v_cvt_pk_bf16_f32 v132, v220, v221
	v_cvt_pk_bf16_f32 v133, v224, v225
	ds_write_b128 v85, v[126:129] offset:7168
	ds_write_b128 v85, v[130:133] offset:7184
	v_cvt_pk_bf16_f32 v126, v5, v7
	v_cvt_pk_bf16_f32 v127, v9, v11
	v_cvt_pk_bf16_f32 v128, v13, v15
	v_cvt_pk_bf16_f32 v129, v17, v69
	v_lshl_add_u32 v5, v207, 2, s3
	v_cvt_pk_bf16_f32 v130, v67, v71
	v_cvt_pk_bf16_f32 v131, v73, v75
	v_cvt_pk_bf16_f32 v132, v77, v79
	v_cvt_pk_bf16_f32 v133, v81, v83
	ds_write_b128 v85, v[126:129] offset:10240
	ds_write_b128 v85, v[130:133] offset:10256
	ds_write_b32 v5, v84 offset:12288
	v_and_b32_e32 v114, 15, v206
	v_mov_b32_e32 v5, v51
	s_nop 1
	v_permlane32_swap_b32_e32 v51, v5
	v_mov_b32_e32 v7, v51
	s_nop 1
	v_permlane16_swap_b32_e32 v51, v7
	v_cmp_eq_u32_e32 vcc, 0, v114
	s_nop 0
	v_mov_b32_dpp v84, v51 row_newbcast:0 row_mask:0xf bank_mask:0xf bound_ctrl:1
	v_cndmask_b32_e32 v87, 0, v7, vcc
	v_pk_fma_f32 v[84:85], v[2:3], v[84:85], v[86:87] op_sel_hi:[1,0,1]
	v_mov_b32_e32 v7, v52
	s_nop 1
	v_permlane32_swap_b32_e32 v52, v7
	v_mov_b32_e32 v9, v52
	s_nop 1
	v_permlane16_swap_b32_e32 v52, v9
	v_cmp_gt_u32_e64 s[40:41], 2, v114
	s_nop 0
	v_mov_b32_dpp v86, v52 row_newbcast:0 row_mask:0xf bank_mask:0xf bound_ctrl:1
	v_mov_b32_dpp v52, v52 row_newbcast:1 row_mask:0xf bank_mask:0xf bound_ctrl:1
	v_cndmask_b32_e64 v91, 0, v9, s[40:41]
	v_pk_fma_f32 v[86:87], v[2:3], v[86:87], v[90:91] op_sel_hi:[1,0,1]
	s_nop 0
	v_pk_fma_f32 v[86:87], v[84:85], v[52:53], v[86:87] op_sel_hi:[1,0,1]
	v_mov_b32_e32 v9, v53
	s_nop 1
	v_permlane32_swap_b32_e32 v53, v9
	v_mov_b32_e32 v11, v53
	s_nop 1
	v_permlane16_swap_b32_e32 v53, v11
	v_cmp_gt_u32_e64 s[42:43], 3, v114
	s_nop 0
	v_readlane_b32 s70, v53, 0
	v_readlane_b32 s72, v53, 1
	v_cndmask_b32_e64 v89, 0, v11, s[42:43]
	v_pk_fma_f32 v[88:89], v[2:3], s[70:71], v[88:89] op_sel_hi:[1,0,1]
	s_nop 0
	v_pk_fma_f32 v[88:89], v[84:85], s[72:73], v[88:89] op_sel_hi:[1,0,1]
	s_nop 0
	v_mov_b32_dpp v52, v53 row_newbcast:2 row_mask:0xf bank_mask:0xf bound_ctrl:1
	v_pk_fma_f32 v[52:53], v[86:87], v[52:53], v[88:89] op_sel_hi:[1,0,1]
	v_mov_b32_e32 v11, v50
	s_nop 1
	v_permlane32_swap_b32_e32 v50, v11
	v_mov_b32_e32 v13, v11
	s_nop 1
	v_permlane16_swap_b32_e32 v11, v13
	v_cmp_gt_u32_e64 s[44:45], 4, v114
	s_nop 0
	v_mov_b32_dpp v50, v11 row_newbcast:0 row_mask:0xf bank_mask:0xf bound_ctrl:1
	v_readlane_b32 s70, v11, 1
	v_readlane_b32 s72, v11, 2
	v_cndmask_b32_e64 v95, 0, v13, s[44:45]
	v_pk_fma_f32 v[50:51], v[2:3], v[50:51], v[94:95] op_sel_hi:[1,0,1]
	s_nop 0
	v_readlane_b32 s74, v11, 3
	v_pk_fma_f32 v[50:51], v[84:85], s[70:71], v[50:51] op_sel_hi:[1,0,1]
	s_nop 0
	v_pk_fma_f32 v[50:51], v[86:87], s[72:73], v[50:51] op_sel_hi:[1,0,1]
	s_nop 0
	s_nop 0
	v_pk_fma_f32 v[50:51], v[52:53], s[74:75], v[50:51] op_sel_hi:[1,0,1]
	v_mov_b32_e32 v11, v5
	s_nop 1
	v_permlane16_swap_b32_e32 v5, v11
	v_cmp_gt_u32_e64 s[46:47], 5, v114
	s_nop 0
	v_mov_b32_dpp v88, v5 row_newbcast:0 row_mask:0xf bank_mask:0xf bound_ctrl:1
	v_readlane_b32 s70, v5, 1
	v_readlane_b32 s72, v5, 2
	v_cndmask_b32_e64 v93, 0, v11, s[46:47]
	v_pk_fma_f32 v[88:89], v[2:3], v[88:89], v[92:93] op_sel_hi:[1,0,1]
	s_nop 0
	v_readlane_b32 s74, v5, 3
	v_pk_fma_f32 v[88:89], v[84:85], s[70:71], v[88:89] op_sel_hi:[1,0,1]
	s_nop 0
	v_readlane_b32 s98, v5, 4
	v_pk_fma_f32 v[88:89], v[86:87], s[72:73], v[88:89] op_sel_hi:[1,0,1]
	s_nop 0
	s_nop 0
	v_pk_fma_f32 v[88:89], v[52:53], s[74:75], v[88:89] op_sel_hi:[1,0,1]
	s_nop 0
	s_nop 0
	v_pk_fma_f32 v[88:89], v[50:51], s[98:99], v[88:89] op_sel_hi:[1,0,1]
	v_mov_b32_e32 v5, v7
	s_nop 1
	v_permlane16_swap_b32_e32 v7, v5
	v_cmp_gt_u32_e64 s[48:49], 6, v114
	s_nop 0
	v_mov_b32_dpp v90, v7 row_newbcast:0 row_mask:0xf bank_mask:0xf bound_ctrl:1
	v_readlane_b32 s70, v7, 1
	v_readlane_b32 s72, v7, 2
	v_cndmask_b32_e64 v119, 0, v5, s[48:49]
	v_pk_fma_f32 v[90:91], v[2:3], v[90:91], v[118:119] op_sel_hi:[1,0,1]
	s_nop 0
	v_readlane_b32 s74, v7, 3
	v_pk_fma_f32 v[90:91], v[84:85], s[70:71], v[90:91] op_sel_hi:[1,0,1]
	s_nop 0
	v_readlane_b32 s98, v7, 4
	v_pk_fma_f32 v[90:91], v[86:87], s[72:73], v[90:91] op_sel_hi:[1,0,1]
	s_nop 0
	s_nop 0
	v_readlane_b32 s70, v7, 5
	v_pk_fma_f32 v[90:91], v[52:53], s[74:75], v[90:91] op_sel_hi:[1,0,1]
	s_nop 0
	s_nop 0
	v_pk_fma_f32 v[90:91], v[50:51], s[98:99], v[90:91] op_sel_hi:[1,0,1]
	s_nop 0
	s_nop 0
	v_pk_fma_f32 v[90:91], v[88:89], s[70:71], v[90:91] op_sel_hi:[1,0,1]
	v_mov_b32_e32 v5, v9
	s_nop 1
	v_permlane16_swap_b32_e32 v9, v5
	v_cmp_gt_u32_e64 s[50:51], 7, v114
	s_nop 0
	v_mov_b32_dpp v92, v9 row_newbcast:0 row_mask:0xf bank_mask:0xf bound_ctrl:1
	v_readlane_b32 s70, v9, 1
	v_readlane_b32 s72, v9, 2
	v_cndmask_b32_e64 v97, 0, v5, s[50:51]
	v_pk_fma_f32 v[92:93], v[2:3], v[92:93], v[96:97] op_sel_hi:[1,0,1]
	s_nop 0
	v_readlane_b32 s74, v9, 3
	v_pk_fma_f32 v[92:93], v[84:85], s[70:71], v[92:93] op_sel_hi:[1,0,1]
	s_nop 0
	v_readlane_b32 s98, v9, 4
	v_pk_fma_f32 v[92:93], v[86:87], s[72:73], v[92:93] op_sel_hi:[1,0,1]
	s_nop 0
	s_nop 0
	v_readlane_b32 s70, v9, 5
	v_pk_fma_f32 v[92:93], v[52:53], s[74:75], v[92:93] op_sel_hi:[1,0,1]
	s_nop 0
	s_nop 0
	v_readlane_b32 s72, v9, 6
	v_pk_fma_f32 v[92:93], v[50:51], s[98:99], v[92:93] op_sel_hi:[1,0,1]
	s_nop 0
	s_nop 0
	v_pk_fma_f32 v[92:93], v[88:89], s[70:71], v[92:93] op_sel_hi:[1,0,1]
	s_nop 0
	s_nop 0
	v_pk_fma_f32 v[92:93], v[90:91], s[72:73], v[92:93] op_sel_hi:[1,0,1]
	v_mov_b32_e32 v5, v54
	s_nop 1
	v_permlane32_swap_b32_e32 v54, v5
	v_mov_b32_e32 v7, v54
	s_nop 1
	v_permlane16_swap_b32_e32 v54, v7
	v_cmp_gt_u32_e64 s[52:53], 8, v114
	s_nop 0
	v_mov_b32_dpp v94, v54 row_newbcast:0 row_mask:0xf bank_mask:0xf bound_ctrl:1
	v_readlane_b32 s70, v54, 1
	v_readlane_b32 s72, v54, 2
	v_cndmask_b32_e64 v125, 0, v7, s[52:53]
	v_pk_fma_f32 v[94:95], v[2:3], v[94:95], v[124:125] op_sel_hi:[1,0,1]
	s_nop 0
	v_readlane_b32 s74, v54, 3
	v_pk_fma_f32 v[94:95], v[84:85], s[70:71], v[94:95] op_sel_hi:[1,0,1]
	s_nop 0
	v_readlane_b32 s98, v54, 4
	v_pk_fma_f32 v[94:95], v[86:87], s[72:73], v[94:95] op_sel_hi:[1,0,1]
	s_nop 0
	s_nop 0
	v_readlane_b32 s70, v54, 5
	v_pk_fma_f32 v[94:95], v[52:53], s[74:75], v[94:95] op_sel_hi:[1,0,1]
	s_nop 0
	s_nop 0
	v_readlane_b32 s72, v54, 6
	v_pk_fma_f32 v[94:95], v[50:51], s[98:99], v[94:95] op_sel_hi:[1,0,1]
	s_nop 0
	s_nop 0
	v_pk_fma_f32 v[94:95], v[88:89], s[70:71], v[94:95] op_sel_hi:[1,0,1]
	s_nop 0
	s_nop 0
	v_pk_fma_f32 v[94:95], v[90:91], s[72:73], v[94:95] op_sel_hi:[1,0,1]
	v_mov_b32_dpp v54, v54 row_newbcast:7 row_mask:0xf bank_mask:0xf bound_ctrl:1
	v_pk_fma_f32 v[94:95], v[92:93], v[54:55], v[94:95] op_sel_hi:[1,0,1]
	v_mov_b32_e32 v7, v55
	s_nop 1
	v_permlane32_swap_b32_e32 v55, v7
	v_mov_b32_e32 v9, v55
	s_nop 1
	v_permlane16_swap_b32_e32 v55, v9
	v_cmp_gt_u32_e64 s[54:55], 9, v114
	s_nop 0
	v_mov_b32_dpp v54, v55 row_newbcast:0 row_mask:0xf bank_mask:0xf bound_ctrl:1
	v_cndmask_b32_e64 v111, 0, v9, s[54:55]
	v_pk_fma_f32 v[96:97], v[2:3], v[54:55], v[110:111] op_sel_hi:[1,0,1]
	v_readlane_b32 s70, v55, 1
	v_readlane_b32 s72, v55, 2
	v_readlane_b32 s74, v55, 3
	v_pk_fma_f32 v[96:97], v[84:85], s[70:71], v[96:97] op_sel_hi:[1,0,1]
	s_nop 0
	s_nop 0
	v_readlane_b32 s98, v55, 4
	v_pk_fma_f32 v[96:97], v[86:87], s[72:73], v[96:97] op_sel_hi:[1,0,1]
	s_nop 0
	s_nop 0
	v_readlane_b32 s70, v55, 5
	v_pk_fma_f32 v[96:97], v[52:53], s[74:75], v[96:97] op_sel_hi:[1,0,1]
	s_nop 0
	s_nop 0
	v_readlane_b32 s72, v55, 6
	v_pk_fma_f32 v[96:97], v[50:51], s[98:99], v[96:97] op_sel_hi:[1,0,1]
	s_nop 0
	s_nop 0
	v_readlane_b32 s74, v55, 7
	v_pk_fma_f32 v[96:97], v[88:89], s[70:71], v[96:97] op_sel_hi:[1,0,1]
	s_nop 0
	s_nop 0
	v_pk_fma_f32 v[96:97], v[90:91], s[72:73], v[96:97] op_sel_hi:[1,0,1]
	s_nop 0
	s_nop 0
	v_pk_fma_f32 v[96:97], v[92:93], s[74:75], v[96:97] op_sel_hi:[1,0,1]
	s_nop 0
	v_mov_b32_dpp v54, v55 row_newbcast:8 row_mask:0xf bank_mask:0xf bound_ctrl:1
	v_pk_fma_f32 v[54:55], v[94:95], v[54:55], v[96:97] op_sel_hi:[1,0,1]
	v_mov_b32_e32 v9, v56
	s_nop 1
	v_permlane32_swap_b32_e32 v56, v9
	v_mov_b32_e32 v11, v56
	s_nop 1
	v_permlane16_swap_b32_e32 v56, v11
	v_cmp_gt_u32_e64 s[58:59], 10, v114
	s_nop 0
	v_mov_b32_dpp v96, v56 row_newbcast:0 row_mask:0xf bank_mask:0xf bound_ctrl:1
	v_readlane_b32 s70, v56, 1
	v_readlane_b32 s72, v56, 2
	v_cndmask_b32_e64 v121, 0, v11, s[58:59]
	v_pk_fma_f32 v[96:97], v[2:3], v[96:97], v[120:121] op_sel_hi:[1,0,1]
	s_nop 0
	v_readlane_b32 s74, v56, 3
	v_pk_fma_f32 v[96:97], v[84:85], s[70:71], v[96:97] op_sel_hi:[1,0,1]
	s_nop 0
	v_readlane_b32 s98, v56, 4
	v_pk_fma_f32 v[96:97], v[86:87], s[72:73], v[96:97] op_sel_hi:[1,0,1]
	s_nop 0
	s_nop 0
	v_readlane_b32 s70, v56, 5
	v_pk_fma_f32 v[96:97], v[52:53], s[74:75], v[96:97] op_sel_hi:[1,0,1]
	s_nop 0
	s_nop 0
	v_readlane_b32 s72, v56, 6
	v_pk_fma_f32 v[96:97], v[50:51], s[98:99], v[96:97] op_sel_hi:[1,0,1]
	s_nop 0
	s_nop 0
	v_readlane_b32 s74, v56, 7
	v_pk_fma_f32 v[96:97], v[88:89], s[70:71], v[96:97] op_sel_hi:[1,0,1]
	s_nop 0
	s_nop 0
	v_readlane_b32 s98, v56, 8
	v_pk_fma_f32 v[96:97], v[90:91], s[72:73], v[96:97] op_sel_hi:[1,0,1]
	s_nop 0
	s_nop 0
	v_pk_fma_f32 v[96:97], v[92:93], s[74:75], v[96:97] op_sel_hi:[1,0,1]
	s_nop 0
	s_nop 0
	v_pk_fma_f32 v[96:97], v[94:95], s[98:99], v[96:97] op_sel_hi:[1,0,1]
	v_mov_b32_dpp v56, v56 row_newbcast:9 row_mask:0xf bank_mask:0xf bound_ctrl:1
	v_pk_fma_f32 v[96:97], v[54:55], v[56:57], v[96:97] op_sel_hi:[1,0,1]
	v_mov_b32_e32 v11, v57
	s_nop 1
	v_permlane32_swap_b32_e32 v57, v11
	v_mov_b32_e32 v13, v57
	s_nop 1
	v_permlane16_swap_b32_e32 v57, v13
	v_cmp_gt_u32_e64 s[62:63], 11, v114
	s_nop 0
	v_readlane_b32 s70, v57, 0
	v_readlane_b32 s72, v57, 1
	v_cndmask_b32_e64 v103, 0, v13, s[62:63]
	v_readlane_b32 s74, v57, 2
	v_pk_fma_f32 v[102:103], v[2:3], s[70:71], v[102:103] op_sel_hi:[1,0,1]
	s_nop 0
	v_readlane_b32 s98, v57, 3
	v_pk_fma_f32 v[102:103], v[84:85], s[72:73], v[102:103] op_sel_hi:[1,0,1]
	s_nop 0
	s_nop 0
	v_readlane_b32 s70, v57, 4
	v_pk_fma_f32 v[102:103], v[86:87], s[74:75], v[102:103] op_sel_hi:[1,0,1]
	s_nop 0
	s_nop 0
	v_readlane_b32 s72, v57, 5
	v_pk_fma_f32 v[102:103], v[52:53], s[98:99], v[102:103] op_sel_hi:[1,0,1]
	s_nop 0
	s_nop 0
	v_readlane_b32 s74, v57, 6
	v_pk_fma_f32 v[102:103], v[50:51], s[70:71], v[102:103] op_sel_hi:[1,0,1]
	s_nop 0
	s_nop 0
	v_readlane_b32 s98, v57, 7
	v_pk_fma_f32 v[102:103], v[88:89], s[72:73], v[102:103] op_sel_hi:[1,0,1]
	s_nop 0
	s_nop 0
	v_readlane_b32 s70, v57, 8
	v_pk_fma_f32 v[102:103], v[90:91], s[74:75], v[102:103] op_sel_hi:[1,0,1]
	s_nop 0
	s_nop 0
	v_readlane_b32 s72, v57, 9
	v_pk_fma_f32 v[102:103], v[92:93], s[98:99], v[102:103] op_sel_hi:[1,0,1]
	s_nop 0
	s_nop 0
	v_pk_fma_f32 v[102:103], v[94:95], s[70:71], v[102:103] op_sel_hi:[1,0,1]
	s_nop 0
	s_nop 0
	v_pk_fma_f32 v[102:103], v[54:55], s[72:73], v[102:103] op_sel_hi:[1,0,1]
	s_nop 0
	v_mov_b32_dpp v56, v57 row_newbcast:10 row_mask:0xf bank_mask:0xf bound_ctrl:1
	v_pk_fma_f32 v[56:57], v[96:97], v[56:57], v[102:103] op_sel_hi:[1,0,1]
	v_mov_b32_e32 v13, v5
	s_nop 1
	v_permlane16_swap_b32_e32 v5, v13
	v_cmp_gt_u32_e64 s[56:57], 12, v114
	s_nop 0
	v_mov_b32_dpp v102, v5 row_newbcast:0 row_mask:0xf bank_mask:0xf bound_ctrl:1
	v_readlane_b32 s70, v5, 1
	v_readlane_b32 s72, v5, 2
	v_cndmask_b32_e64 v113, 0, v13, s[56:57]
	v_pk_fma_f32 v[102:103], v[2:3], v[102:103], v[112:113] op_sel_hi:[1,0,1]
	s_nop 0
	v_readlane_b32 s74, v5, 3
	v_pk_fma_f32 v[102:103], v[84:85], s[70:71], v[102:103] op_sel_hi:[1,0,1]
	s_nop 0
	v_readlane_b32 s98, v5, 4
	v_pk_fma_f32 v[102:103], v[86:87], s[72:73], v[102:103] op_sel_hi:[1,0,1]
	s_nop 0
	s_nop 0
	v_readlane_b32 s70, v5, 5
	v_pk_fma_f32 v[102:103], v[52:53], s[74:75], v[102:103] op_sel_hi:[1,0,1]
	s_nop 0
	s_nop 0
	v_readlane_b32 s72, v5, 6
	v_pk_fma_f32 v[102:103], v[50:51], s[98:99], v[102:103] op_sel_hi:[1,0,1]
	s_nop 0
	s_nop 0
	v_readlane_b32 s74, v5, 7
	v_pk_fma_f32 v[102:103], v[88:89], s[70:71], v[102:103] op_sel_hi:[1,0,1]
	s_nop 0
	s_nop 0
	v_readlane_b32 s98, v5, 8
	v_pk_fma_f32 v[102:103], v[90:91], s[72:73], v[102:103] op_sel_hi:[1,0,1]
	s_nop 0
	s_nop 0
	v_readlane_b32 s70, v5, 9
	v_pk_fma_f32 v[102:103], v[92:93], s[74:75], v[102:103] op_sel_hi:[1,0,1]
	s_nop 0
	s_nop 0
	v_readlane_b32 s72, v5, 10
	v_pk_fma_f32 v[102:103], v[94:95], s[98:99], v[102:103] op_sel_hi:[1,0,1]
	s_nop 0
	s_nop 0
	v_readlane_b32 s74, v5, 11
	v_pk_fma_f32 v[102:103], v[54:55], s[70:71], v[102:103] op_sel_hi:[1,0,1]
	s_nop 0
	s_nop 0
	v_pk_fma_f32 v[102:103], v[96:97], s[72:73], v[102:103] op_sel_hi:[1,0,1]
	s_nop 0
	s_nop 0
	v_pk_fma_f32 v[102:103], v[56:57], s[74:75], v[102:103] op_sel_hi:[1,0,1]
	v_mov_b32_e32 v5, v7
	s_nop 1
	v_permlane16_swap_b32_e32 v7, v5
	v_cmp_gt_u32_e64 s[60:61], 13, v114
	s_nop 0
	v_readlane_b32 s70, v7, 0
	v_readlane_b32 s72, v7, 1
	v_cndmask_b32_e64 v105, 0, v5, s[60:61]
	v_readlane_b32 s74, v7, 2
	v_pk_fma_f32 v[104:105], v[2:3], s[70:71], v[104:105] op_sel_hi:[1,0,1]
	s_nop 0
	v_readlane_b32 s98, v7, 3
	v_pk_fma_f32 v[104:105], v[84:85], s[72:73], v[104:105] op_sel_hi:[1,0,1]
	s_nop 0
	s_nop 0
	v_readlane_b32 s70, v7, 4
	v_pk_fma_f32 v[104:105], v[86:87], s[74:75], v[104:105] op_sel_hi:[1,0,1]
	s_nop 0
	s_nop 0
	v_readlane_b32 s72, v7, 5
	v_pk_fma_f32 v[104:105], v[52:53], s[98:99], v[104:105] op_sel_hi:[1,0,1]
	s_nop 0
	s_nop 0
	v_readlane_b32 s74, v7, 6
	v_pk_fma_f32 v[104:105], v[50:51], s[70:71], v[104:105] op_sel_hi:[1,0,1]
	s_nop 0
	s_nop 0
	v_readlane_b32 s98, v7, 7
	v_pk_fma_f32 v[104:105], v[88:89], s[72:73], v[104:105] op_sel_hi:[1,0,1]
	s_nop 0
	s_nop 0
	v_readlane_b32 s70, v7, 8
	v_pk_fma_f32 v[104:105], v[90:91], s[74:75], v[104:105] op_sel_hi:[1,0,1]
	s_nop 0
	s_nop 0
	v_readlane_b32 s72, v7, 9
	v_pk_fma_f32 v[104:105], v[92:93], s[98:99], v[104:105] op_sel_hi:[1,0,1]
	s_nop 0
	s_nop 0
	v_readlane_b32 s74, v7, 10
	v_pk_fma_f32 v[104:105], v[94:95], s[70:71], v[104:105] op_sel_hi:[1,0,1]
	s_nop 0
	s_nop 0
	v_readlane_b32 s98, v7, 11
	v_pk_fma_f32 v[104:105], v[54:55], s[72:73], v[104:105] op_sel_hi:[1,0,1]
	s_nop 0
	s_nop 0
	v_readlane_b32 s70, v7, 12
	v_pk_fma_f32 v[104:105], v[96:97], s[74:75], v[104:105] op_sel_hi:[1,0,1]
	s_nop 0
	s_nop 0
	v_pk_fma_f32 v[104:105], v[56:57], s[98:99], v[104:105] op_sel_hi:[1,0,1]
	s_nop 0
	s_nop 0
	v_pk_fma_f32 v[104:105], v[102:103], s[70:71], v[104:105] op_sel_hi:[1,0,1]
	v_mov_b32_e32 v5, v9
	s_nop 1
	v_permlane16_swap_b32_e32 v9, v5
	v_cmp_gt_u32_e64 s[64:65], 14, v114
	s_nop 0
	v_readlane_b32 s70, v9, 0
	v_readlane_b32 s72, v9, 1
	v_cndmask_b32_e64 v107, 0, v5, s[64:65]
	v_readlane_b32 s74, v9, 2
	v_pk_fma_f32 v[106:107], v[2:3], s[70:71], v[106:107] op_sel_hi:[1,0,1]
	s_nop 0
	v_readlane_b32 s98, v9, 3
	v_pk_fma_f32 v[106:107], v[84:85], s[72:73], v[106:107] op_sel_hi:[1,0,1]
	s_nop 0
	s_nop 0
	v_readlane_b32 s70, v9, 4
	v_pk_fma_f32 v[106:107], v[86:87], s[74:75], v[106:107] op_sel_hi:[1,0,1]
	s_nop 0
	s_nop 0
	v_readlane_b32 s72, v9, 5
	v_pk_fma_f32 v[106:107], v[52:53], s[98:99], v[106:107] op_sel_hi:[1,0,1]
	s_nop 0
	s_nop 0
	v_readlane_b32 s74, v9, 6
	v_pk_fma_f32 v[106:107], v[50:51], s[70:71], v[106:107] op_sel_hi:[1,0,1]
	s_nop 0
	s_nop 0
	v_readlane_b32 s98, v9, 7
	v_pk_fma_f32 v[106:107], v[88:89], s[72:73], v[106:107] op_sel_hi:[1,0,1]
	s_nop 0
	s_nop 0
	v_readlane_b32 s70, v9, 8
	v_pk_fma_f32 v[106:107], v[90:91], s[74:75], v[106:107] op_sel_hi:[1,0,1]
	s_nop 0
	s_nop 0
	v_readlane_b32 s72, v9, 9
	v_pk_fma_f32 v[106:107], v[92:93], s[98:99], v[106:107] op_sel_hi:[1,0,1]
	s_nop 0
	s_nop 0
	v_readlane_b32 s74, v9, 10
	v_pk_fma_f32 v[106:107], v[94:95], s[70:71], v[106:107] op_sel_hi:[1,0,1]
	s_nop 0
	s_nop 0
	v_readlane_b32 s98, v9, 11
	v_pk_fma_f32 v[106:107], v[54:55], s[72:73], v[106:107] op_sel_hi:[1,0,1]
	s_nop 0
	s_nop 0
	v_readlane_b32 s70, v9, 12
	v_pk_fma_f32 v[106:107], v[96:97], s[74:75], v[106:107] op_sel_hi:[1,0,1]
	s_nop 0
	s_nop 0
	v_readlane_b32 s72, v9, 13
	v_pk_fma_f32 v[106:107], v[56:57], s[98:99], v[106:107] op_sel_hi:[1,0,1]
	s_nop 0
	s_nop 0
	v_pk_fma_f32 v[106:107], v[102:103], s[70:71], v[106:107] op_sel_hi:[1,0,1]
	s_nop 0
	s_nop 0
	v_pk_fma_f32 v[106:107], v[104:105], s[72:73], v[106:107] op_sel_hi:[1,0,1]
	v_mov_b32_e32 v5, v11
	s_nop 1
	v_permlane16_swap_b32_e32 v11, v5
	v_cmp_eq_u32_e64 s[66:67], 15, v114
	s_nop 0
	v_readlane_b32 s70, v11, 0
	v_readlane_b32 s72, v11, 1
	v_cndmask_b32_e64 v109, v5, 0, s[66:67]
	v_readlane_b32 s74, v11, 2
	v_pk_fma_f32 v[108:109], v[2:3], s[70:71], v[108:109] op_sel_hi:[1,0,1]
	s_nop 0
	v_readlane_b32 s98, v11, 3
	v_pk_fma_f32 v[108:109], v[84:85], s[72:73], v[108:109] op_sel_hi:[1,0,1]
	s_nop 0
	s_nop 0
	v_readlane_b32 s70, v11, 4
	v_pk_fma_f32 v[108:109], v[86:87], s[74:75], v[108:109] op_sel_hi:[1,0,1]
	s_nop 0
	s_nop 0
	v_readlane_b32 s72, v11, 5
	v_pk_fma_f32 v[108:109], v[52:53], s[98:99], v[108:109] op_sel_hi:[1,0,1]
	s_nop 0
	s_nop 0
	v_readlane_b32 s74, v11, 6
	v_pk_fma_f32 v[108:109], v[50:51], s[70:71], v[108:109] op_sel_hi:[1,0,1]
	s_nop 0
	s_nop 0
	v_readlane_b32 s98, v11, 7
	v_pk_fma_f32 v[108:109], v[88:89], s[72:73], v[108:109] op_sel_hi:[1,0,1]
	s_nop 0
	s_nop 0
	v_readlane_b32 s70, v11, 8
	v_pk_fma_f32 v[108:109], v[90:91], s[74:75], v[108:109] op_sel_hi:[1,0,1]
	s_nop 0
	s_nop 0
	v_readlane_b32 s72, v11, 9
	v_pk_fma_f32 v[108:109], v[92:93], s[98:99], v[108:109] op_sel_hi:[1,0,1]
	s_nop 0
	s_nop 0
	v_readlane_b32 s74, v11, 10
	v_pk_fma_f32 v[108:109], v[94:95], s[70:71], v[108:109] op_sel_hi:[1,0,1]
	s_nop 0
	s_nop 0
	v_readlane_b32 s98, v11, 11
	v_pk_fma_f32 v[108:109], v[54:55], s[72:73], v[108:109] op_sel_hi:[1,0,1]
	s_nop 0
	s_nop 0
	v_readlane_b32 s70, v11, 12
	v_pk_fma_f32 v[108:109], v[96:97], s[74:75], v[108:109] op_sel_hi:[1,0,1]
	s_nop 0
	s_nop 0
	v_readlane_b32 s72, v11, 13
	v_pk_fma_f32 v[108:109], v[56:57], s[98:99], v[108:109] op_sel_hi:[1,0,1]
	s_nop 0
	s_nop 0
	v_pk_fma_f32 v[108:109], v[102:103], s[70:71], v[108:109] op_sel_hi:[1,0,1]
	s_nop 0
	s_nop 0
	v_pk_fma_f32 v[108:109], v[104:105], s[72:73], v[108:109] op_sel_hi:[1,0,1]
	s_nop 0
	v_mov_b32_dpp v110, v11 row_newbcast:14 row_mask:0xf bank_mask:0xf bound_ctrl:1
	v_pk_fma_f32 v[108:109], v[106:107], v[110:111], v[108:109] op_sel_hi:[1,0,1]
	v_mov_b32_e32 v5, v58
	s_nop 1
	v_permlane32_swap_b32_e32 v58, v5
	v_mov_b32_e32 v7, v58
	s_nop 1
	v_permlane16_swap_b32_e32 v58, v7
	v_cndmask_b32_e32 v83, 0, v7, vcc
	s_nop 0
	v_mov_b32_dpp v58, v58 row_newbcast:0 row_mask:0xf bank_mask:0xf bound_ctrl:1
	v_pk_fma_f32 v[82:83], v[2:3], v[58:59], v[82:83] op_sel_hi:[1,0,1]
	v_mov_b32_e32 v7, v59
	s_nop 1
	v_permlane32_swap_b32_e32 v59, v7
	v_mov_b32_e32 v9, v59
	s_nop 1
	v_permlane16_swap_b32_e32 v59, v9
	v_cndmask_b32_e64 v81, 0, v9, s[40:41]
	s_nop 0
	v_readlane_b32 s70, v59, 0
	s_nop 1
	v_pk_fma_f32 v[80:81], v[2:3], s[70:71], v[80:81] op_sel_hi:[1,0,1]
	s_nop 0
	v_mov_b32_dpp v58, v59 row_newbcast:1 row_mask:0xf bank_mask:0xf bound_ctrl:1
	v_pk_fma_f32 v[58:59], v[84:85], v[58:59], v[80:81] op_sel_hi:[1,0,1]
	v_mov_b32_e32 v9, v60
	s_nop 1
	v_permlane32_swap_b32_e32 v60, v9
	v_mov_b32_e32 v11, v60
	s_nop 1
	v_permlane16_swap_b32_e32 v60, v11
	v_cndmask_b32_e64 v79, 0, v11, s[42:43]
	s_nop 0
	v_readlane_b32 s70, v60, 0
	s_nop 1
	v_pk_fma_f32 v[78:79], v[2:3], s[70:71], v[78:79] op_sel_hi:[1,0,1]
	s_nop 0
	v_mov_b32_dpp v80, v60 row_newbcast:1 row_mask:0xf bank_mask:0xf bound_ctrl:1
	v_pk_fma_f32 v[78:79], v[84:85], v[80:81], v[78:79] op_sel_hi:[1,0,1]
	v_mov_b32_dpp v60, v60 row_newbcast:2 row_mask:0xf bank_mask:0xf bound_ctrl:1
	v_pk_fma_f32 v[78:79], v[86:87], v[60:61], v[78:79] op_sel_hi:[1,0,1]
	v_mov_b32_e32 v11, v61
	s_nop 1
	v_permlane32_swap_b32_e32 v61, v11
	v_mov_b32_e32 v13, v61
	s_nop 1
	v_permlane16_swap_b32_e32 v61, v13
	v_cndmask_b32_e64 v77, 0, v13, s[44:45]
	s_nop 0
	v_readlane_b32 s70, v61, 0
	v_readlane_b32 s72, v61, 1
	v_readlane_b32 s74, v61, 2
	v_pk_fma_f32 v[76:77], v[2:3], s[70:71], v[76:77] op_sel_hi:[1,0,1]
	s_nop 0
	s_nop 0
	v_pk_fma_f32 v[76:77], v[84:85], s[72:73], v[76:77] op_sel_hi:[1,0,1]
	s_nop 0
	s_nop 0
	v_pk_fma_f32 v[76:77], v[86:87], s[74:75], v[76:77] op_sel_hi:[1,0,1]
	s_nop 0
	v_mov_b32_dpp v60, v61 row_newbcast:3 row_mask:0xf bank_mask:0xf bound_ctrl:1
	v_pk_fma_f32 v[60:61], v[52:53], v[60:61], v[76:77] op_sel_hi:[1,0,1]
	v_mov_b32_e32 v13, v5
	s_nop 1
	v_permlane16_swap_b32_e32 v5, v13
	v_cndmask_b32_e64 v75, 0, v13, s[46:47]
	s_nop 0
	v_readlane_b32 s70, v5, 0
	v_readlane_b32 s72, v5, 1
	v_readlane_b32 s74, v5, 2
	v_pk_fma_f32 v[74:75], v[2:3], s[70:71], v[74:75] op_sel_hi:[1,0,1]
	s_nop 0
	s_nop 0
	v_readlane_b32 s98, v5, 3
	v_pk_fma_f32 v[74:75], v[84:85], s[72:73], v[74:75] op_sel_hi:[1,0,1]
	s_nop 0
	s_nop 0
	v_readlane_b32 s70, v5, 4
	v_pk_fma_f32 v[74:75], v[86:87], s[74:75], v[74:75] op_sel_hi:[1,0,1]
	s_nop 0
	s_nop 0
	v_pk_fma_f32 v[74:75], v[52:53], s[98:99], v[74:75] op_sel_hi:[1,0,1]
	s_nop 0
	s_nop 0
	v_pk_fma_f32 v[74:75], v[50:51], s[70:71], v[74:75] op_sel_hi:[1,0,1]
	v_mov_b32_e32 v5, v7
	s_nop 1
	v_permlane16_swap_b32_e32 v7, v5
	v_cndmask_b32_e64 v73, 0, v5, s[48:49]
	s_nop 0
	v_readlane_b32 s70, v7, 0
	v_readlane_b32 s72, v7, 1
	v_readlane_b32 s74, v7, 2
	v_pk_fma_f32 v[72:73], v[2:3], s[70:71], v[72:73] op_sel_hi:[1,0,1]
	s_nop 0
	s_nop 0
	v_readlane_b32 s98, v7, 3
	v_pk_fma_f32 v[72:73], v[84:85], s[72:73], v[72:73] op_sel_hi:[1,0,1]
	s_nop 0
	s_nop 0
	v_readlane_b32 s70, v7, 4
	v_pk_fma_f32 v[72:73], v[86:87], s[74:75], v[72:73] op_sel_hi:[1,0,1]
	s_nop 0
	s_nop 0
	v_readlane_b32 s72, v7, 5
	v_pk_fma_f32 v[72:73], v[52:53], s[98:99], v[72:73] op_sel_hi:[1,0,1]
	s_nop 0
	s_nop 0
	v_pk_fma_f32 v[72:73], v[50:51], s[70:71], v[72:73] op_sel_hi:[1,0,1]
	s_nop 0
	s_nop 0
	v_pk_fma_f32 v[72:73], v[88:89], s[72:73], v[72:73] op_sel_hi:[1,0,1]
	v_mov_b32_e32 v5, v9
	s_nop 1
	v_permlane16_swap_b32_e32 v9, v5
	v_cndmask_b32_e64 v71, 0, v5, s[50:51]
	s_nop 0
	v_readlane_b32 s70, v9, 0
	v_readlane_b32 s72, v9, 1
	v_readlane_b32 s74, v9, 2
	v_pk_fma_f32 v[70:71], v[2:3], s[70:71], v[70:71] op_sel_hi:[1,0,1]
	s_nop 0
	s_nop 0
	v_readlane_b32 s98, v9, 3
	v_pk_fma_f32 v[70:71], v[84:85], s[72:73], v[70:71] op_sel_hi:[1,0,1]
	s_nop 0
	s_nop 0
	v_readlane_b32 s70, v9, 4
	v_pk_fma_f32 v[70:71], v[86:87], s[74:75], v[70:71] op_sel_hi:[1,0,1]
	s_nop 0
	s_nop 0
	v_readlane_b32 s72, v9, 5
	v_pk_fma_f32 v[70:71], v[52:53], s[98:99], v[70:71] op_sel_hi:[1,0,1]
	s_nop 0
	s_nop 0
	v_readlane_b32 s74, v9, 6
	v_pk_fma_f32 v[70:71], v[50:51], s[70:71], v[70:71] op_sel_hi:[1,0,1]
	s_nop 0
	s_nop 0
	v_pk_fma_f32 v[70:71], v[88:89], s[72:73], v[70:71] op_sel_hi:[1,0,1]
	s_nop 0
	s_nop 0
	v_pk_fma_f32 v[70:71], v[90:91], s[74:75], v[70:71] op_sel_hi:[1,0,1]
	v_mov_b32_e32 v5, v11
	s_nop 1
	v_permlane16_swap_b32_e32 v11, v5
	v_cndmask_b32_e64 v69, 0, v5, s[52:53]
	s_nop 0
	v_readlane_b32 s70, v11, 0
	v_readlane_b32 s72, v11, 1
	v_readlane_b32 s74, v11, 2
	v_pk_fma_f32 v[68:69], v[2:3], s[70:71], v[68:69] op_sel_hi:[1,0,1]
	s_nop 0
	s_nop 0
	v_readlane_b32 s98, v11, 3
	v_pk_fma_f32 v[68:69], v[84:85], s[72:73], v[68:69] op_sel_hi:[1,0,1]
	s_nop 0
	s_nop 0
	v_readlane_b32 s70, v11, 4
	v_pk_fma_f32 v[68:69], v[86:87], s[74:75], v[68:69] op_sel_hi:[1,0,1]
	s_nop 0
	s_nop 0
	v_readlane_b32 s72, v11, 5
	v_pk_fma_f32 v[68:69], v[52:53], s[98:99], v[68:69] op_sel_hi:[1,0,1]
	s_nop 0
	s_nop 0
	v_readlane_b32 s74, v11, 6
	v_pk_fma_f32 v[68:69], v[50:51], s[70:71], v[68:69] op_sel_hi:[1,0,1]
	s_nop 0
	s_nop 0
	v_readlane_b32 s98, v11, 7
	v_pk_fma_f32 v[68:69], v[88:89], s[72:73], v[68:69] op_sel_hi:[1,0,1]
	s_nop 0
	s_nop 0
	v_pk_fma_f32 v[68:69], v[90:91], s[74:75], v[68:69] op_sel_hi:[1,0,1]
	s_nop 0
	s_nop 0
	v_pk_fma_f32 v[68:69], v[92:93], s[98:99], v[68:69] op_sel_hi:[1,0,1]
	v_mov_b32_e32 v5, v62
	s_nop 1
	v_permlane32_swap_b32_e32 v62, v5
	v_mov_b32_e32 v7, v62
	s_nop 1
	v_permlane16_swap_b32_e32 v62, v7
	v_cndmask_b32_e64 v67, 0, v7, s[54:55]
	s_nop 0
	v_readlane_b32 s70, v62, 0
	v_readlane_b32 s72, v62, 1
	v_readlane_b32 s74, v62, 2
	v_pk_fma_f32 v[66:67], v[2:3], s[70:71], v[66:67] op_sel_hi:[1,0,1]
	s_nop 0
	s_nop 0
	v_readlane_b32 s98, v62, 3
	v_pk_fma_f32 v[66:67], v[84:85], s[72:73], v[66:67] op_sel_hi:[1,0,1]
	s_nop 0
	s_nop 0
	v_readlane_b32 s70, v62, 4
	v_pk_fma_f32 v[66:67], v[86:87], s[74:75], v[66:67] op_sel_hi:[1,0,1]
	s_nop 0
	s_nop 0
	v_readlane_b32 s72, v62, 5
	v_pk_fma_f32 v[66:67], v[52:53], s[98:99], v[66:67] op_sel_hi:[1,0,1]
	s_nop 0
	s_nop 0
	v_readlane_b32 s74, v62, 6
	v_pk_fma_f32 v[66:67], v[50:51], s[70:71], v[66:67] op_sel_hi:[1,0,1]
	s_nop 0
	s_nop 0
	v_pk_fma_f32 v[66:67], v[88:89], s[72:73], v[66:67] op_sel_hi:[1,0,1]
	s_nop 0
	s_nop 0
	v_pk_fma_f32 v[66:67], v[90:91], s[74:75], v[66:67] op_sel_hi:[1,0,1]
	s_nop 0
	v_mov_b32_dpp v76, v62 row_newbcast:7 row_mask:0xf bank_mask:0xf bound_ctrl:1
	v_pk_fma_f32 v[66:67], v[92:93], v[76:77], v[66:67] op_sel_hi:[1,0,1]
	v_mov_b32_dpp v62, v62 row_newbcast:8 row_mask:0xf bank_mask:0xf bound_ctrl:1
	v_pk_fma_f32 v[66:67], v[94:95], v[62:63], v[66:67] op_sel_hi:[1,0,1]
	v_mov_b32_e32 v7, v63
	s_nop 1
	v_permlane32_swap_b32_e32 v63, v7
	v_mov_b32_e32 v9, v63
	s_nop 1
	v_permlane16_swap_b32_e32 v63, v9
	v_cndmask_b32_e64 v17, 0, v9, s[58:59]
	s_nop 0
	v_readlane_b32 s70, v63, 0
	v_readlane_b32 s72, v63, 1
	v_readlane_b32 s74, v63, 2
	v_pk_fma_f32 v[16:17], v[2:3], s[70:71], v[16:17] op_sel_hi:[1,0,1]
	s_nop 0
	s_nop 0
	v_readlane_b32 s98, v63, 3
	v_pk_fma_f32 v[16:17], v[84:85], s[72:73], v[16:17] op_sel_hi:[1,0,1]
	s_nop 0
	s_nop 0
	v_readlane_b32 s70, v63, 4
	v_pk_fma_f32 v[16:17], v[86:87], s[74:75], v[16:17] op_sel_hi:[1,0,1]
	s_nop 0
	s_nop 0
	v_readlane_b32 s72, v63, 5
	v_pk_fma_f32 v[16:17], v[52:53], s[98:99], v[16:17] op_sel_hi:[1,0,1]
	s_nop 0
	s_nop 0
	v_readlane_b32 s74, v63, 6
	v_pk_fma_f32 v[16:17], v[50:51], s[70:71], v[16:17] op_sel_hi:[1,0,1]
	s_nop 0
	s_nop 0
	v_readlane_b32 s98, v63, 7
	v_pk_fma_f32 v[16:17], v[88:89], s[72:73], v[16:17] op_sel_hi:[1,0,1]
	s_nop 0
	s_nop 0
	v_readlane_b32 s70, v63, 8
	v_pk_fma_f32 v[16:17], v[90:91], s[74:75], v[16:17] op_sel_hi:[1,0,1]
	s_nop 0
	s_nop 0
	v_readlane_b32 s72, v63, 9
	v_pk_fma_f32 v[16:17], v[92:93], s[98:99], v[16:17] op_sel_hi:[1,0,1]
	s_nop 0
	s_nop 0
	v_pk_fma_f32 v[16:17], v[94:95], s[70:71], v[16:17] op_sel_hi:[1,0,1]
	s_nop 0
	s_nop 0
	v_pk_fma_f32 v[16:17], v[54:55], s[72:73], v[16:17] op_sel_hi:[1,0,1]
	v_mov_b32_e32 v63, v64
	s_nop 1
	v_permlane32_swap_b32_e32 v64, v63
	v_mov_b32_e32 v9, v64
	s_nop 1
	v_permlane16_swap_b32_e32 v64, v9
	v_cndmask_b32_e64 v15, 0, v9, s[62:63]
	s_nop 0
	v_readlane_b32 s70, v64, 0
	v_readlane_b32 s72, v64, 1
	v_readlane_b32 s74, v64, 2
	v_pk_fma_f32 v[14:15], v[2:3], s[70:71], v[14:15] op_sel_hi:[1,0,1]
	s_nop 0
	s_nop 0
	v_readlane_b32 s98, v64, 3
	v_pk_fma_f32 v[14:15], v[84:85], s[72:73], v[14:15] op_sel_hi:[1,0,1]
	s_nop 0
	s_nop 0
	v_readlane_b32 s70, v64, 4
	v_pk_fma_f32 v[14:15], v[86:87], s[74:75], v[14:15] op_sel_hi:[1,0,1]
	s_nop 0
	s_nop 0
	v_readlane_b32 s72, v64, 5
	v_pk_fma_f32 v[14:15], v[52:53], s[98:99], v[14:15] op_sel_hi:[1,0,1]
	s_nop 0
	s_nop 0
	v_readlane_b32 s74, v64, 6
	v_pk_fma_f32 v[14:15], v[50:51], s[70:71], v[14:15] op_sel_hi:[1,0,1]
	s_nop 0
	s_nop 0
	v_readlane_b32 s98, v64, 7
	v_pk_fma_f32 v[14:15], v[88:89], s[72:73], v[14:15] op_sel_hi:[1,0,1]
	s_nop 0
	s_nop 0
	v_readlane_b32 s70, v64, 8
	v_pk_fma_f32 v[14:15], v[90:91], s[74:75], v[14:15] op_sel_hi:[1,0,1]
	s_nop 0
	s_nop 0
	v_readlane_b32 s72, v64, 9
	v_pk_fma_f32 v[14:15], v[92:93], s[98:99], v[14:15] op_sel_hi:[1,0,1]
	s_nop 0
	s_nop 0
	v_readlane_b32 s74, v64, 10
	v_pk_fma_f32 v[14:15], v[94:95], s[70:71], v[14:15] op_sel_hi:[1,0,1]
	s_nop 0
	s_nop 0
	v_pk_fma_f32 v[14:15], v[54:55], s[72:73], v[14:15] op_sel_hi:[1,0,1]
	s_nop 0
	s_nop 0
	v_pk_fma_f32 v[14:15], v[96:97], s[74:75], v[14:15] op_sel_hi:[1,0,1]
	v_mov_b32_e32 v64, v65
	s_nop 1
	v_permlane32_swap_b32_e32 v65, v64
	v_mov_b32_e32 v9, v65
	s_nop 1
	v_permlane16_swap_b32_e32 v65, v9
	v_cndmask_b32_e64 v13, 0, v9, s[56:57]
	s_nop 0
	v_readlane_b32 s70, v65, 0
	v_readlane_b32 s72, v65, 1
	v_readlane_b32 s74, v65, 2
	v_pk_fma_f32 v[12:13], v[2:3], s[70:71], v[12:13] op_sel_hi:[1,0,1]
	s_nop 0
	s_nop 0
	v_readlane_b32 s98, v65, 3
	v_pk_fma_f32 v[12:13], v[84:85], s[72:73], v[12:13] op_sel_hi:[1,0,1]
	s_nop 0
	s_nop 0
	v_readlane_b32 s70, v65, 4
	v_pk_fma_f32 v[12:13], v[86:87], s[74:75], v[12:13] op_sel_hi:[1,0,1]
	s_nop 0
	s_nop 0
	v_readlane_b32 s72, v65, 5
	v_pk_fma_f32 v[12:13], v[52:53], s[98:99], v[12:13] op_sel_hi:[1,0,1]
	s_nop 0
	s_nop 0
	v_readlane_b32 s74, v65, 6
	v_pk_fma_f32 v[12:13], v[50:51], s[70:71], v[12:13] op_sel_hi:[1,0,1]
	s_nop 0
	s_nop 0
	v_readlane_b32 s98, v65, 7
	v_pk_fma_f32 v[12:13], v[88:89], s[72:73], v[12:13] op_sel_hi:[1,0,1]
	s_nop 0
	s_nop 0
	v_readlane_b32 s70, v65, 8
	v_pk_fma_f32 v[12:13], v[90:91], s[74:75], v[12:13] op_sel_hi:[1,0,1]
	s_nop 0
	s_nop 0
	v_readlane_b32 s72, v65, 9
	v_pk_fma_f32 v[12:13], v[92:93], s[98:99], v[12:13] op_sel_hi:[1,0,1]
	s_nop 0
	s_nop 0
	v_readlane_b32 s74, v65, 10
	v_pk_fma_f32 v[12:13], v[94:95], s[70:71], v[12:13] op_sel_hi:[1,0,1]
	s_nop 0
	s_nop 0
	v_readlane_b32 s98, v65, 11
	v_pk_fma_f32 v[12:13], v[54:55], s[72:73], v[12:13] op_sel_hi:[1,0,1]
	s_nop 0
	s_nop 0
	v_pk_fma_f32 v[12:13], v[96:97], s[74:75], v[12:13] op_sel_hi:[1,0,1]
	s_nop 0
	s_nop 0
	v_pk_fma_f32 v[12:13], v[56:57], s[98:99], v[12:13] op_sel_hi:[1,0,1]
	v_mov_b32_e32 v9, v5
	s_nop 1
	v_permlane16_swap_b32_e32 v5, v9
	v_cndmask_b32_e64 v11, 0, v9, s[60:61]
	s_nop 0
	v_readlane_b32 s70, v5, 0
	v_readlane_b32 s72, v5, 1
	v_readlane_b32 s74, v5, 2
	v_pk_fma_f32 v[10:11], v[2:3], s[70:71], v[10:11] op_sel_hi:[1,0,1]
	s_nop 0
	s_nop 0
	v_readlane_b32 s98, v5, 3
	v_pk_fma_f32 v[10:11], v[84:85], s[72:73], v[10:11] op_sel_hi:[1,0,1]
	s_nop 0
	s_nop 0
	v_readlane_b32 s70, v5, 4
	v_pk_fma_f32 v[10:11], v[86:87], s[74:75], v[10:11] op_sel_hi:[1,0,1]
	s_nop 0
	s_nop 0
	v_readlane_b32 s72, v5, 5
	v_pk_fma_f32 v[10:11], v[52:53], s[98:99], v[10:11] op_sel_hi:[1,0,1]
	s_nop 0
	s_nop 0
	v_readlane_b32 s74, v5, 6
	v_pk_fma_f32 v[10:11], v[50:51], s[70:71], v[10:11] op_sel_hi:[1,0,1]
	s_nop 0
	s_nop 0
	v_readlane_b32 s98, v5, 7
	v_pk_fma_f32 v[10:11], v[88:89], s[72:73], v[10:11] op_sel_hi:[1,0,1]
	s_nop 0
	s_nop 0
	v_readlane_b32 s70, v5, 8
	v_pk_fma_f32 v[10:11], v[90:91], s[74:75], v[10:11] op_sel_hi:[1,0,1]
	s_nop 0
	s_nop 0
	v_readlane_b32 s72, v5, 9
	v_pk_fma_f32 v[10:11], v[92:93], s[98:99], v[10:11] op_sel_hi:[1,0,1]
	s_nop 0
	s_nop 0
	v_readlane_b32 s74, v5, 10
	v_pk_fma_f32 v[10:11], v[94:95], s[70:71], v[10:11] op_sel_hi:[1,0,1]
	s_nop 0
	s_nop 0
	v_readlane_b32 s98, v5, 11
	v_pk_fma_f32 v[10:11], v[54:55], s[72:73], v[10:11] op_sel_hi:[1,0,1]
	s_nop 0
	s_nop 0
	v_readlane_b32 s70, v5, 12
	v_pk_fma_f32 v[10:11], v[96:97], s[74:75], v[10:11] op_sel_hi:[1,0,1]
	s_nop 0
	s_nop 0
	v_pk_fma_f32 v[10:11], v[56:57], s[98:99], v[10:11] op_sel_hi:[1,0,1]
	s_nop 0
	s_nop 0
	v_pk_fma_f32 v[10:11], v[102:103], s[70:71], v[10:11] op_sel_hi:[1,0,1]
	v_mov_b32_e32 v5, v7
	s_nop 1
	v_permlane16_swap_b32_e32 v7, v5
	v_cndmask_b32_e64 v9, 0, v5, s[64:65]
	s_nop 0
	v_readlane_b32 s70, v7, 0
	v_readlane_b32 s72, v7, 1
	v_readlane_b32 s74, v7, 2
	v_pk_fma_f32 v[8:9], v[2:3], s[70:71], v[8:9] op_sel_hi:[1,0,1]
	s_nop 0
	s_nop 0
	v_readlane_b32 s98, v7, 3
	v_pk_fma_f32 v[8:9], v[84:85], s[72:73], v[8:9] op_sel_hi:[1,0,1]
	s_nop 0
	s_nop 0
	v_readlane_b32 s70, v7, 4
	v_pk_fma_f32 v[8:9], v[86:87], s[74:75], v[8:9] op_sel_hi:[1,0,1]
	s_nop 0
	s_nop 0
	v_readlane_b32 s72, v7, 5
	v_pk_fma_f32 v[8:9], v[52:53], s[98:99], v[8:9] op_sel_hi:[1,0,1]
	s_nop 0
	s_nop 0
	v_readlane_b32 s74, v7, 6
	v_pk_fma_f32 v[8:9], v[50:51], s[70:71], v[8:9] op_sel_hi:[1,0,1]
	s_nop 0
	s_nop 0
	v_readlane_b32 s98, v7, 7
	v_pk_fma_f32 v[8:9], v[88:89], s[72:73], v[8:9] op_sel_hi:[1,0,1]
	s_nop 0
	s_nop 0
	v_readlane_b32 s70, v7, 8
	v_pk_fma_f32 v[8:9], v[90:91], s[74:75], v[8:9] op_sel_hi:[1,0,1]
	s_nop 0
	s_nop 0
	v_readlane_b32 s72, v7, 9
	v_pk_fma_f32 v[8:9], v[92:93], s[98:99], v[8:9] op_sel_hi:[1,0,1]
	s_nop 0
	s_nop 0
	v_readlane_b32 s74, v7, 10
	v_pk_fma_f32 v[8:9], v[94:95], s[70:71], v[8:9] op_sel_hi:[1,0,1]
	s_nop 0
	s_nop 0
	v_readlane_b32 s98, v7, 11
	v_pk_fma_f32 v[8:9], v[54:55], s[72:73], v[8:9] op_sel_hi:[1,0,1]
	s_nop 0
	s_nop 0
	v_readlane_b32 s70, v7, 12
	v_pk_fma_f32 v[8:9], v[96:97], s[74:75], v[8:9] op_sel_hi:[1,0,1]
	s_nop 0
	s_nop 0
	v_readlane_b32 s72, v7, 13
	v_pk_fma_f32 v[8:9], v[56:57], s[98:99], v[8:9] op_sel_hi:[1,0,1]
	s_nop 0
	s_nop 0
	v_pk_fma_f32 v[8:9], v[102:103], s[70:71], v[8:9] op_sel_hi:[1,0,1]
	s_nop 0
	s_nop 0
	v_pk_fma_f32 v[8:9], v[104:105], s[72:73], v[8:9] op_sel_hi:[1,0,1]
	v_mov_b32_e32 v5, v63
	s_nop 1
	v_permlane16_swap_b32_e32 v63, v5
	v_cndmask_b32_e64 v7, v5, 0, s[66:67]
	s_nop 0
	v_readlane_b32 s70, v63, 0
	v_readlane_b32 s72, v63, 1
	v_readlane_b32 s74, v63, 2
	v_pk_fma_f32 v[6:7], v[2:3], s[70:71], v[6:7] op_sel_hi:[1,0,1]
	s_nop 0
	s_nop 0
	v_readlane_b32 s98, v63, 3
	v_pk_fma_f32 v[6:7], v[84:85], s[72:73], v[6:7] op_sel_hi:[1,0,1]
	s_nop 0
	s_nop 0
	v_readlane_b32 s70, v63, 4
	v_pk_fma_f32 v[6:7], v[86:87], s[74:75], v[6:7] op_sel_hi:[1,0,1]
	s_nop 0
	s_nop 0
	v_readlane_b32 s72, v63, 5
	v_pk_fma_f32 v[6:7], v[52:53], s[98:99], v[6:7] op_sel_hi:[1,0,1]
	s_nop 0
	s_nop 0
	v_readlane_b32 s74, v63, 6
	v_pk_fma_f32 v[6:7], v[50:51], s[70:71], v[6:7] op_sel_hi:[1,0,1]
	s_nop 0
	s_nop 0
	v_readlane_b32 s98, v63, 7
	v_pk_fma_f32 v[6:7], v[88:89], s[72:73], v[6:7] op_sel_hi:[1,0,1]
	s_nop 0
	s_nop 0
	v_readlane_b32 s70, v63, 8
	v_pk_fma_f32 v[6:7], v[90:91], s[74:75], v[6:7] op_sel_hi:[1,0,1]
	s_nop 0
	s_nop 0
	v_readlane_b32 s72, v63, 9
	v_pk_fma_f32 v[6:7], v[92:93], s[98:99], v[6:7] op_sel_hi:[1,0,1]
	s_nop 0
	s_nop 0
	v_readlane_b32 s74, v63, 10
	v_pk_fma_f32 v[6:7], v[94:95], s[70:71], v[6:7] op_sel_hi:[1,0,1]
	s_nop 0
	s_nop 0
	v_readlane_b32 s98, v63, 11
	v_pk_fma_f32 v[6:7], v[54:55], s[72:73], v[6:7] op_sel_hi:[1,0,1]
	s_nop 0
	s_nop 0
	v_readlane_b32 s70, v63, 12
	v_pk_fma_f32 v[6:7], v[96:97], s[74:75], v[6:7] op_sel_hi:[1,0,1]
	s_nop 0
	s_nop 0
	v_readlane_b32 s72, v63, 13
	v_pk_fma_f32 v[6:7], v[56:57], s[98:99], v[6:7] op_sel_hi:[1,0,1]
	s_nop 0
	s_nop 0
	v_readlane_b32 s74, v63, 14
	v_pk_fma_f32 v[6:7], v[102:103], s[70:71], v[6:7] op_sel_hi:[1,0,1]
	s_nop 0
	s_nop 0
	v_pk_fma_f32 v[6:7], v[104:105], s[72:73], v[6:7] op_sel_hi:[1,0,1]
	s_nop 0
	s_nop 0
	v_pk_fma_f32 v[6:7], v[106:107], s[74:75], v[6:7] op_sel_hi:[1,0,1]
	v_mov_b32_e32 v5, v64
	s_nop 1
	v_permlane16_swap_b32_e32 v64, v5
	s_nop 1
	v_readlane_b32 s70, v64, 0
	v_readlane_b32 s72, v64, 1
	v_readlane_b32 s74, v64, 2
	v_pk_fma_f32 v[4:5], v[2:3], s[70:71], v[4:5] op_sel_hi:[1,0,1]
	s_nop 0
	v_readlane_b32 s98, v64, 3
	v_pk_fma_f32 v[4:5], v[84:85], s[72:73], v[4:5] op_sel_hi:[1,0,1]
	s_nop 0
	s_nop 0
	v_readlane_b32 s70, v64, 4
	v_pk_fma_f32 v[4:5], v[86:87], s[74:75], v[4:5] op_sel_hi:[1,0,1]
	s_nop 0
	s_nop 0
	v_readlane_b32 s72, v64, 5
	v_pk_fma_f32 v[4:5], v[52:53], s[98:99], v[4:5] op_sel_hi:[1,0,1]
	s_nop 0
	s_nop 0
	v_readlane_b32 s74, v64, 6
	v_pk_fma_f32 v[4:5], v[50:51], s[70:71], v[4:5] op_sel_hi:[1,0,1]
	s_nop 0
	s_nop 0
	v_readlane_b32 s98, v64, 7
	v_pk_fma_f32 v[4:5], v[88:89], s[72:73], v[4:5] op_sel_hi:[1,0,1]
	s_nop 0
	s_nop 0
	v_readlane_b32 s70, v64, 8
	v_pk_fma_f32 v[4:5], v[90:91], s[74:75], v[4:5] op_sel_hi:[1,0,1]
	s_nop 0
	s_nop 0
	v_readlane_b32 s72, v64, 9
	v_pk_fma_f32 v[4:5], v[92:93], s[98:99], v[4:5] op_sel_hi:[1,0,1]
	s_nop 0
	s_nop 0
	v_readlane_b32 s74, v64, 10
	v_pk_fma_f32 v[4:5], v[94:95], s[70:71], v[4:5] op_sel_hi:[1,0,1]
	s_nop 0
	s_nop 0
	v_readlane_b32 s98, v64, 11
	v_pk_fma_f32 v[4:5], v[54:55], s[72:73], v[4:5] op_sel_hi:[1,0,1]
	s_nop 0
	s_nop 0
	v_readlane_b32 s70, v64, 12
	v_pk_fma_f32 v[4:5], v[96:97], s[74:75], v[4:5] op_sel_hi:[1,0,1]
	s_nop 0
	s_nop 0
	v_readlane_b32 s72, v64, 13
	v_pk_fma_f32 v[4:5], v[56:57], s[98:99], v[4:5] op_sel_hi:[1,0,1]
	s_nop 0
	s_nop 0
	v_readlane_b32 s74, v64, 14
	v_pk_fma_f32 v[4:5], v[102:103], s[70:71], v[4:5] op_sel_hi:[1,0,1]
	s_nop 0
	s_nop 0
	v_readlane_b32 s98, v64, 15
	v_pk_fma_f32 v[4:5], v[104:105], s[72:73], v[4:5] op_sel_hi:[1,0,1]
	s_nop 0
	s_nop 0
	v_pk_fma_f32 v[4:5], v[106:107], s[74:75], v[4:5] op_sel_hi:[1,0,1]
	s_nop 0
	s_nop 0
	v_pk_fma_f32 v[4:5], v[108:109], s[98:99], v[4:5] op_sel_hi:[1,0,1]
	v_and_b32_e32 v2, 48, v206
	v_and_or_b32 v2, v208, 8, v2
	v_and_b32_e32 v62, 8, v206
	v_and_or_b32 v62, v208, 6, v62
	v_lshlrev_b32_e32 v2, 1, v2
	v_add3_u32 v63, s3, v2, v62
	v_cvt_pk_bf16_f32 v64, v82, s0
	ds_write_b16 v63, v64 offset:3072
	v_xor_b32_e32 v64, 16, v2
	v_add3_u32 v64, s3, v64, v62
	v_cvt_pk_bf16_f32 v58, v58, s0
	v_cvt_pk_bf16_f32 v65, v84, s0
	ds_write_b16 v64, v58 offset:3200
	v_xor_b32_e32 v58, 32, v2
	ds_write_b16 v64, v65 offset:1152
	v_add3_u32 v58, s3, v58, v62
	v_cvt_pk_bf16_f32 v65, v86, s0
	ds_write_b16 v58, v65 offset:1280
	v_cvt_pk_bf16_f32 v65, v78, s0
	ds_write_b16 v58, v65 offset:3328
	v_xor_b32_e32 v65, 48, v2
	v_add3_u32 v65, s3, v65, v62
	v_cvt_pk_bf16_f32 v52, v52, s0
	ds_write_b16 v65, v52 offset:1408
	v_cvt_pk_bf16_f32 v52, v60, s0
	ds_write_b16 v65, v52 offset:3456
	v_xor_b32_e32 v52, 64, v2
	v_add3_u32 v52, s3, v52, v62
	v_cvt_pk_bf16_f32 v50, v50, s0
	ds_write_b16 v52, v50 offset:1536
	v_cvt_pk_bf16_f32 v50, v74, s0
	ds_write_b16 v52, v50 offset:3584
	v_xor_b32_e32 v50, 0x50, v2
	v_add3_u32 v50, s3, v50, v62
	v_cvt_pk_bf16_f32 v60, v88, s0
	ds_write_b16 v50, v60 offset:1664
	v_cvt_pk_bf16_f32 v60, v72, s0
	ds_write_b16 v50, v60 offset:3712
	v_xor_b32_e32 v60, 0x60, v2
	v_xor_b32_e32 v2, 0x70, v2
	v_add3_u32 v60, s3, v60, v62
	v_add3_u32 v2, s3, v2, v62
	v_cvt_pk_bf16_f32 v62, v92, s0
	ds_write_b16 v2, v62 offset:1920
	v_cvt_pk_bf16_f32 v62, v68, s0
	ds_write_b16 v2, v62 offset:3968
	v_cvt_pk_bf16_f32 v62, v94, s0
	v_cvt_pk_bf16_f32 v16, v16, s0
	v_cvt_pk_bf16_f32 v14, v14, s0
	v_cvt_pk_bf16_f32 v12, v12, s0
	v_cvt_pk_bf16_f32 v10, v10, s0
	v_cvt_pk_bf16_f32 v8, v8, s0
	v_cvt_pk_bf16_f32 v6, v6, s0
	v_cvt_pk_bf16_f32 v72, v90, s0
	v_cvt_pk_bf16_f32 v70, v70, s0
	ds_write_b16 v63, v62 offset:2048
	v_cvt_pk_bf16_f32 v62, v66, s0
	v_cvt_pk_bf16_f32 v54, v54, s0
	ds_write_b16 v64, v16 offset:4224
	v_cvt_pk_bf16_f32 v16, v96, s0
	ds_write_b16 v58, v14 offset:4352
	v_cvt_pk_bf16_f32 v14, v56, s0
	ds_write_b16 v65, v12 offset:4480
	v_cvt_pk_bf16_f32 v12, v102, s0
	ds_write_b16 v52, v10 offset:4608
	v_cvt_pk_bf16_f32 v10, v104, s0
	ds_write_b16 v50, v8 offset:4736
	v_cvt_pk_bf16_f32 v8, v106, s0
	ds_write_b16 v60, v6 offset:4864
	v_cvt_pk_bf16_f32 v6, v108, s0
	v_cvt_pk_bf16_f32 v4, v4, s0
	v_cmp_gt_u32_e32 vcc, 16, v207
	ds_write_b16 v63, v209 offset:1024
	ds_write_b16 v60, v72 offset:1792
	ds_write_b16 v60, v70 offset:3840
	ds_write_b16 v63, v62 offset:4096
	ds_write_b16 v64, v54 offset:2176
	ds_write_b16 v58, v16 offset:2304
	ds_write_b16 v65, v14 offset:2432
	ds_write_b16 v52, v12 offset:2560
	ds_write_b16 v50, v10 offset:2688
	ds_write_b16 v60, v8 offset:2816
	ds_write_b16 v2, v6 offset:2944
	ds_write_b16 v2, v4 offset:4992
	s_and_saveexec_b64 s[0:1], vcc
	s_cbranch_execz .LBB0_682
	v_lshl_add_u32 v2, v114, 1, s3
	v_cvt_pk_bf16_f32 v4, v83, s0
	ds_write_b16 v2, v4 offset:9728
	v_cvt_pk_bf16_f32 v4, v85, s0
	ds_write_b16 v2, v4 offset:9248
	v_cvt_pk_bf16_f32 v4, v59, s0
	ds_write_b16 v2, v4 offset:9760
	v_cvt_pk_bf16_f32 v4, v87, s0
	ds_write_b16 v2, v4 offset:9280
	v_cvt_pk_bf16_f32 v4, v79, s0
	ds_write_b16 v2, v4 offset:9792
	v_cvt_pk_bf16_f32 v4, v53, s0
	ds_write_b16 v2, v4 offset:9312
	v_cvt_pk_bf16_f32 v4, v61, s0
	ds_write_b16 v2, v4 offset:9824
	v_cvt_pk_bf16_f32 v4, v51, s0
	ds_write_b16 v2, v4 offset:9344
	v_cvt_pk_bf16_f32 v4, v75, s0
	ds_write_b16 v2, v4 offset:9856
	v_cvt_pk_bf16_f32 v4, v89, s0
	ds_write_b16 v2, v4 offset:9376
	v_cvt_pk_bf16_f32 v4, v73, s0
	ds_write_b16 v2, v4 offset:9888
	v_cvt_pk_bf16_f32 v4, v91, s0
	ds_write_b16 v2, v4 offset:9408
	v_cvt_pk_bf16_f32 v4, v71, s0
	ds_write_b16 v2, v4 offset:9920
	v_cvt_pk_bf16_f32 v4, v93, s0
	ds_write_b16 v2, v4 offset:9440
	v_cvt_pk_bf16_f32 v4, v69, s0
	ds_write_b16 v2, v4 offset:9952
	v_cvt_pk_bf16_f32 v4, v95, s0
	ds_write_b16 v2, v4 offset:9472
	v_cvt_pk_bf16_f32 v4, v67, s0
	ds_write_b16 v2, v4 offset:9984
	v_cvt_pk_bf16_f32 v4, v55, s0
	ds_write_b16 v2, v4 offset:9504
	v_cvt_pk_bf16_f32 v4, v17, s0
	ds_write_b16 v2, v4 offset:10016
	v_cvt_pk_bf16_f32 v4, v97, s0
	ds_write_b16 v2, v4 offset:9536
	v_cvt_pk_bf16_f32 v4, v15, s0
	ds_write_b16 v2, v4 offset:10048
	v_cvt_pk_bf16_f32 v4, v57, s0
	ds_write_b16 v2, v4 offset:9568
	v_cvt_pk_bf16_f32 v4, v13, s0
	ds_write_b16 v2, v4 offset:10080
	v_cvt_pk_bf16_f32 v4, v103, s0
	ds_write_b16 v2, v4 offset:9600
	v_cvt_pk_bf16_f32 v4, v11, s0
	ds_write_b16 v2, v4 offset:10112
	v_cvt_pk_bf16_f32 v4, v105, s0
	ds_write_b16 v2, v4 offset:9632
	v_cvt_pk_bf16_f32 v4, v9, s0
	ds_write_b16 v2, v4 offset:10144
	v_cvt_pk_bf16_f32 v4, v107, s0
	ds_write_b16 v2, v4 offset:9664
	v_cvt_pk_bf16_f32 v4, v7, s0
	ds_write_b16 v2, v4 offset:10176
	v_cvt_pk_bf16_f32 v4, v109, s0
	ds_write_b16 v2, v4 offset:9696
	v_cvt_pk_bf16_f32 v4, v5, s0
	ds_write_b16 v2, v3 offset:9216
	ds_write_b16 v2, v4 offset:10208
.LBB0_682:
	v_readlane_b32 s70, v255, 50
	v_readlane_b32 s71, v255, 51
	v_readlane_b32 s72, v255, 52
	v_readlane_b32 s73, v255, 53
	v_readlane_b32 s74, v255, 54
	v_readlane_b32 s75, v255, 55
	s_or_b64 exec, exec, s[0:1]
	s_cmpk_gt_u32 s6, 0x109
	s_cbranch_scc1 .LBB0_673
	s_lshl_b32 s0, s6, 4
	s_add_i32 s1, s0, 0x60
	s_add_i32 s3, s0, 0xffffff60
	s_add_i32 s41, s0, 0x61
	s_add_i32 s40, s0, 0xffffff61
	s_cmp_lt_u32 s6, 10
	s_movk_i32 s6, 0x9f
	s_cselect_b32 s6, s6, 0x109f
	s_cselect_b32 s3, s1, s3
	s_movk_i32 s1, 0x10ff
	s_cselect_b32 s42, s87, s37
	s_cselect_b32 s43, 0xff, s1
	s_cselect_b32 s44, s41, s40
	s_sub_i32 s6, s6, s0
	s_and_b64 s[0:1], s[38:39], exec
	s_cselect_b32 s3, s3, s6
	s_add_i32 s40, s3, s42
	s_sub_i32 s6, s43, s41
	v_mov_b32_e32 v2, v0
	s_and_b64 s[0:1], s[38:39], exec
	s_cselect_b32 s0, s44, s6
	v_and_or_b32 v4, v2, 63, s36
	s_add_i32 s42, s0, s42
	v_ashrrev_i32_e32 v5, 31, v4
	v_lshlrev_b64 v[4:5], 1, v[4:5]
	s_ashr_i32 s41, s40, 31
	s_ashr_i32 s43, s42, 31
	v_lshl_add_u64 v[12:13], s[88:89], 0, v[4:5]
	s_lshl_b64 s[44:45], s[40:41], 11
	s_lshl_b64 s[42:43], s[42:43], 11
	v_lshl_add_u64 v[10:11], s[90:91], 0, v[4:5]
	v_lshl_add_u64 v[14:15], v[12:13], 0, s[44:45]
	v_lshl_add_u64 v[16:17], v[12:13], 0, s[42:43]
	v_lshl_add_u64 v[8:9], s[26:27], 0, v[4:5]
	global_load_ushort v140, v[14:15], off
	global_load_ushort v142, v[16:17], off
	v_lshl_add_u64 v[14:15], v[10:11], 0, s[44:45]
	v_lshl_add_u64 v[6:7], s[78:79], 0, v[4:5]
	global_load_ushort v2, v[14:15], off
	v_lshl_add_u64 v[14:15], v[8:9], 0, s[44:45]
	s_sub_i32 s0, s0, s3
	v_lshl_add_u64 v[4:5], s[8:9], 0, v[4:5]
	global_load_ushort v141, v[14:15], off
	v_lshl_add_u64 v[14:15], v[6:7], 0, s[44:45]
	global_load_ushort v143, v[14:15], off
	v_lshl_add_u64 v[14:15], v[4:5], 0, s[44:45]
	v_lshl_add_u64 v[16:17], v[10:11], 0, s[42:43]
	s_lshl_b32 s1, s0, 1
	global_load_ushort v14, v[14:15], off
	s_add_i32 s40, s1, s40
	global_load_ushort v15, v[16:17], off
	v_lshl_add_u64 v[16:17], v[8:9], 0, s[42:43]
	global_load_ushort v144, v[16:17], off
	v_lshl_add_u64 v[16:17], v[6:7], 0, s[42:43]
	s_ashr_i32 s41, s40, 31
	global_load_ushort v145, v[16:17], off
	v_lshl_add_u64 v[16:17], v[4:5], 0, s[42:43]
	s_lshl_b64 s[42:43], s[40:41], 11
	v_lshl_add_u64 v[50:51], v[12:13], 0, s[42:43]
	global_load_ushort v16, v[16:17], off
	s_add_i32 s40, s40, s0
	global_load_ushort v146, v[50:51], off
	v_lshl_add_u64 v[50:51], v[10:11], 0, s[42:43]
	global_load_ushort v17, v[50:51], off
	v_lshl_add_u64 v[50:51], v[8:9], 0, s[42:43]
	global_load_ushort v147, v[50:51], off
	v_lshl_add_u64 v[50:51], v[6:7], 0, s[42:43]
	s_ashr_i32 s41, s40, 31
	global_load_ushort v148, v[50:51], off
	v_lshl_add_u64 v[50:51], v[4:5], 0, s[42:43]
	s_lshl_b64 s[42:43], s[40:41], 11
	v_lshl_add_u64 v[52:53], v[12:13], 0, s[42:43]
	global_load_ushort v50, v[50:51], off
	s_add_i32 s40, s40, s0
	global_load_ushort v149, v[52:53], off
	v_lshl_add_u64 v[52:53], v[10:11], 0, s[42:43]
	global_load_ushort v51, v[52:53], off
	v_lshl_add_u64 v[52:53], v[8:9], 0, s[42:43]
	global_load_ushort v150, v[52:53], off
	v_lshl_add_u64 v[52:53], v[6:7], 0, s[42:43]
	s_ashr_i32 s41, s40, 31
	global_load_ushort v152, v[52:53], off
	v_lshl_add_u64 v[52:53], v[4:5], 0, s[42:43]
	s_lshl_b64 s[42:43], s[40:41], 11
	v_lshl_add_u64 v[54:55], v[12:13], 0, s[42:43]
	global_load_ushort v52, v[52:53], off
	s_add_i32 s40, s40, s0
	global_load_ushort v151, v[54:55], off
	v_lshl_add_u64 v[54:55], v[10:11], 0, s[42:43]
	global_load_ushort v53, v[54:55], off
	v_lshl_add_u64 v[54:55], v[8:9], 0, s[42:43]
	global_load_ushort v153, v[54:55], off
	v_lshl_add_u64 v[54:55], v[6:7], 0, s[42:43]
	s_ashr_i32 s41, s40, 31
	global_load_ushort v155, v[54:55], off
	v_lshl_add_u64 v[54:55], v[4:5], 0, s[42:43]
	s_lshl_b64 s[42:43], s[40:41], 11
	v_lshl_add_u64 v[56:57], v[12:13], 0, s[42:43]
	global_load_ushort v54, v[54:55], off
	s_add_i32 s40, s40, s0
	global_load_ushort v154, v[56:57], off
	v_lshl_add_u64 v[56:57], v[10:11], 0, s[42:43]
	global_load_ushort v55, v[56:57], off
	v_lshl_add_u64 v[56:57], v[8:9], 0, s[42:43]
	global_load_ushort v156, v[56:57], off
	v_lshl_add_u64 v[56:57], v[6:7], 0, s[42:43]
	s_ashr_i32 s41, s40, 31
	global_load_ushort v158, v[56:57], off
	v_lshl_add_u64 v[56:57], v[4:5], 0, s[42:43]
	s_lshl_b64 s[42:43], s[40:41], 11
	v_lshl_add_u64 v[58:59], v[12:13], 0, s[42:43]
	global_load_ushort v56, v[56:57], off
	s_add_i32 s40, s40, s0
	global_load_ushort v157, v[58:59], off
	v_lshl_add_u64 v[58:59], v[10:11], 0, s[42:43]
	global_load_ushort v57, v[58:59], off
	v_lshl_add_u64 v[58:59], v[8:9], 0, s[42:43]
	global_load_ushort v159, v[58:59], off
	v_lshl_add_u64 v[58:59], v[6:7], 0, s[42:43]
	s_ashr_i32 s41, s40, 31
	global_load_ushort v161, v[58:59], off
	v_lshl_add_u64 v[58:59], v[4:5], 0, s[42:43]
	s_lshl_b64 s[42:43], s[40:41], 11
	global_load_ushort v60, v[58:59], off
	v_lshl_add_u64 v[58:59], v[12:13], 0, s[42:43]
	global_load_ushort v160, v[58:59], off
	v_lshl_add_u64 v[58:59], v[10:11], 0, s[42:43]
	global_load_ushort v61, v[58:59], off
	v_lshl_add_u64 v[58:59], v[8:9], 0, s[42:43]
	s_add_i32 s40, s40, s0
	global_load_ushort v162, v[58:59], off
	v_lshl_add_u64 v[58:59], v[6:7], 0, s[42:43]
	s_ashr_i32 s41, s40, 31
	global_load_ushort v163, v[58:59], off
	v_lshl_add_u64 v[58:59], v[4:5], 0, s[42:43]
	s_lshl_b64 s[42:43], s[40:41], 11
	global_load_ushort v62, v[58:59], off
	v_lshl_add_u64 v[58:59], v[12:13], 0, s[42:43]
	global_load_ushort v164, v[58:59], off
	v_lshl_add_u64 v[58:59], v[10:11], 0, s[42:43]
	global_load_ushort v63, v[58:59], off
	v_lshl_add_u64 v[58:59], v[8:9], 0, s[42:43]
	s_add_i32 s40, s40, s0
	global_load_ushort v165, v[58:59], off
	v_lshl_add_u64 v[58:59], v[6:7], 0, s[42:43]
	s_ashr_i32 s41, s40, 31
	global_load_ushort v167, v[58:59], off
	v_lshl_add_u64 v[58:59], v[4:5], 0, s[42:43]
	s_lshl_b64 s[42:43], s[40:41], 11
	global_load_ushort v64, v[58:59], off
	v_lshl_add_u64 v[58:59], v[12:13], 0, s[42:43]
	global_load_ushort v166, v[58:59], off
	v_lshl_add_u64 v[58:59], v[10:11], 0, s[42:43]
	global_load_ushort v65, v[58:59], off
	v_lshl_add_u64 v[58:59], v[8:9], 0, s[42:43]
	s_add_i32 s40, s40, s0
	global_load_ushort v168, v[58:59], off
	v_lshl_add_u64 v[58:59], v[6:7], 0, s[42:43]
	s_ashr_i32 s41, s40, 31
	global_load_ushort v170, v[58:59], off
	v_lshl_add_u64 v[58:59], v[4:5], 0, s[42:43]
	s_lshl_b64 s[42:43], s[40:41], 11
	global_load_ushort v66, v[58:59], off
	v_lshl_add_u64 v[58:59], v[12:13], 0, s[42:43]
	global_load_ushort v169, v[58:59], off
	v_lshl_add_u64 v[58:59], v[10:11], 0, s[42:43]
	global_load_ushort v67, v[58:59], off
	v_lshl_add_u64 v[58:59], v[8:9], 0, s[42:43]
	s_add_i32 s40, s40, s0
	global_load_ushort v171, v[58:59], off
	v_lshl_add_u64 v[58:59], v[6:7], 0, s[42:43]
	s_ashr_i32 s41, s40, 31
	global_load_ushort v172, v[58:59], off
	v_lshl_add_u64 v[58:59], v[4:5], 0, s[42:43]
	s_lshl_b64 s[42:43], s[40:41], 11
	global_load_ushort v68, v[58:59], off
	v_lshl_add_u64 v[58:59], v[12:13], 0, s[42:43]
	global_load_ushort v173, v[58:59], off
	v_lshl_add_u64 v[58:59], v[10:11], 0, s[42:43]
	global_load_ushort v69, v[58:59], off
	v_lshl_add_u64 v[58:59], v[8:9], 0, s[42:43]
	s_add_i32 s40, s40, s0
	global_load_ushort v174, v[58:59], off
	v_lshl_add_u64 v[58:59], v[6:7], 0, s[42:43]
	s_ashr_i32 s41, s40, 31
	global_load_ushort v175, v[58:59], off
	v_lshl_add_u64 v[58:59], v[4:5], 0, s[42:43]
	s_lshl_b64 s[42:43], s[40:41], 11
	global_load_ushort v70, v[58:59], off
	v_lshl_add_u64 v[58:59], v[12:13], 0, s[42:43]
	global_load_ushort v176, v[58:59], off
	v_lshl_add_u64 v[58:59], v[10:11], 0, s[42:43]
	global_load_ushort v71, v[58:59], off
	v_lshl_add_u64 v[58:59], v[8:9], 0, s[42:43]
	s_add_i32 s40, s40, s0
	global_load_ushort v177, v[58:59], off
	v_lshl_add_u64 v[58:59], v[6:7], 0, s[42:43]
	s_ashr_i32 s41, s40, 31
	global_load_ushort v178, v[58:59], off
	v_lshl_add_u64 v[58:59], v[4:5], 0, s[42:43]
	s_lshl_b64 s[42:43], s[40:41], 11
	global_load_ushort v72, v[58:59], off
	v_lshl_add_u64 v[58:59], v[12:13], 0, s[42:43]
	global_load_ushort v179, v[58:59], off
	v_lshl_add_u64 v[58:59], v[10:11], 0, s[42:43]
	s_add_i32 s40, s40, s0
	global_load_ushort v73, v[58:59], off
	v_lshl_add_u64 v[58:59], v[8:9], 0, s[42:43]
	s_add_i32 s0, s40, s0
	global_load_ushort v180, v[58:59], off
	v_lshl_add_u64 v[58:59], v[6:7], 0, s[42:43]
	s_ashr_i32 s41, s40, 31
	s_ashr_i32 s1, s0, 31
	global_load_ushort v181, v[58:59], off
	v_lshl_add_u64 v[58:59], v[4:5], 0, s[42:43]
	s_lshl_b64 s[42:43], s[40:41], 11
	s_lshl_b64 s[0:1], s[0:1], 11
	global_load_ushort v74, v[58:59], off
	v_lshl_add_u64 v[58:59], v[12:13], 0, s[42:43]
	v_lshl_add_u64 v[12:13], v[12:13], 0, s[0:1]
	global_load_ushort v184, v[58:59], off
	global_load_ushort v187, v[12:13], off
	v_lshl_add_u64 v[58:59], v[10:11], 0, s[42:43]
	global_load_ushort v75, v[58:59], off
	v_lshl_add_u64 v[58:59], v[8:9], 0, s[42:43]
	global_load_ushort v185, v[58:59], off
	v_lshl_add_u64 v[58:59], v[6:7], 0, s[42:43]
	global_load_ushort v186, v[58:59], off
	v_lshl_add_u64 v[58:59], v[4:5], 0, s[42:43]
	v_lshl_add_u64 v[10:11], v[10:11], 0, s[0:1]
	v_lshl_add_u64 v[8:9], v[8:9], 0, s[0:1]
	v_lshl_add_u64 v[6:7], v[6:7], 0, s[0:1]
	v_lshl_add_u64 v[4:5], v[4:5], 0, s[0:1]
	global_load_ushort v58, v[58:59], off
	s_waitcnt vmcnt(39)
	v_perm_b32 v194, v61, v57, s13
	global_load_ushort v10, v[10:11], off
	s_waitcnt vmcnt(37)
	v_perm_b32 v195, v62, v60, s13
	global_load_ushort v188, v[8:9], off
	global_load_ushort v189, v[6:7], off
	v_perm_b32 v196, v55, v53, s13
	global_load_ushort v4, v[4:5], off
	v_perm_b32 v197, v56, v54, s13
	s_waitcnt vmcnt(33)
	v_perm_b32 v200, v65, v63, s13
	s_waitcnt vmcnt(30)
	v_perm_b32 v201, v66, v64, s13
	v_perm_b32 v202, v51, v17, s13
	v_perm_b32 v203, v52, v50, s13
	v_perm_b32 v204, v15, v2, s13
	v_perm_b32 v205, v16, v14, s13
	s_waitcnt vmcnt(23)
	v_perm_b32 v198, v69, v67, s13
	s_waitcnt vmcnt(20)
	v_perm_b32 v199, v70, v68, s13
	s_waitcnt vmcnt(13)
	v_perm_b32 v192, v73, v71, s13
	s_waitcnt vmcnt(10)
	v_perm_b32 v193, v74, v72, s13
	s_waitcnt vmcnt(3)
	v_perm_b32 v190, v10, v75, s13
	s_waitcnt vmcnt(0)
	v_perm_b32 v191, v4, v58, s13
	s_branch .LBB0_673
